# conv-in-NSA with two register sets (second set parked in the idle top-k LDS slab), loads consumed two iterations later, items remapped so one CU writes whole fp8 lines, no drain at unit ends, pipeline
# speedup vs baseline: 1.0212x; 1.0062x over previous
; __device__ __forceinline__ void p0_weights(const Args& a, LAS unsigned char* lds) {
;     ...
;         else if ((r -= I_FD) < 16 * I_MG) { const int up = r / (8 * I_MG); r -= up * 8 * I_MG; const int e = r / I_MG; r -= e * I_MG; W = a.in[up ? I_MWU : I_MWG] + (size_t)e * D * DFE; w.K = D; w.N = DFE;
;             w.dst = a.ws + WS_MGU_T + (size_t)e * 2 * DFE * D * (MOE_FP8 ? 1 : 2); w.kind = 2 + up; w.f8 = MOE_FP8; w.scale = F8_WGU; }
;         else { r -= 16 * I_MG; const int e = r / I_MD; r -= e * I_MD; W = a.in[I_MWD] + (size_t)e * DFE * D; w.K = DFE; w.N = D; w.dst = a.ws + WS_MD_T + (size_t)e * D * DFE * (MOE_FP8 ? 1 : 2); w.f8 = MOE_FP8; w.scale = F8_WD; }
;         const int nblk = (w.N + 31) >> 5, kb = r / nblk, nb = r - kb * nblk;
;         w.k0 = 128 * kb + 16 * (lane >> 3); w.n = 32 * nb + 4 * (lane & 7); w.valid = w.n < w.N; w.src = W + (size_t)w.k0 * w.N + w.n;
; __device__ __forceinline__ void nsa_unit(const Args& a, LAS unsigned char* lds, int b, int kvh, int qb) {
;     ...
; #pragma unroll
;     for (int dt = 0; dt < 4; ++dt)
; #pragma unroll
;         for (int i = 0; i < 16; ++i) o[dt][i] = 0.f;
;     float mrun = -1e30f, lrun = 0.f;
;     f32x16 p0, p1;
; #pragma unroll
;     for (int i = 0; i < 16; ++i) { p0[i] = 0.f; p1[i] = 0.f; }
;     bf16x8 pf[2][2];
;     if (w >= 4) asm volatile("s_barrier" ::: "memory");
.LBB0_894:
	s_cmp_lt_i32 s15, -1
	s_cbranch_scc1 .LBB0_919
	v_mov_b32_e32 v49, v47
	s_lshl_b32 s0, s72, 1
	s_max_i32 s1, s72, 8
	v_mov_b32_e32 v60, v47
	v_mov_b32_e32 v61, v47
	v_lshl_add_u64 v[206:207], s[30:31], 0, v[48:49]
	s_sub_i32 s63, s0, s1
	v_mov_b32_e32 v46, v47
	v_mov_b32_e32 v48, v47
	v_mov_b32_e32 v50, v47
	v_mov_b32_e32 v51, v47
	v_mov_b32_e32 v52, v47
	v_mov_b32_e32 v53, v47
	v_mov_b32_e32 v54, v47
	v_mov_b32_e32 v55, v47
	v_mov_b32_e32 v56, v47
	v_mov_b32_e32 v57, v47
	v_mov_b32_e32 v58, v47
	v_mov_b32_e32 v59, v47
	v_mov_b64_e32 v[108:109], v[60:61]
	v_mov_b64_e32 v[124:125], v[60:61]
	v_mov_b64_e32 v[140:141], v[60:61]
	v_mov_b64_e32 v[156:157], v[60:61]
	v_mov_b64_e32 v[76:77], v[60:61]
	v_mov_b64_e32 v[92:93], v[60:61]
	v_add_u32_e32 v43, 1, v249
	s_add_i32 s23, s63, 11
	s_add_i32 s24, s63, 10
	s_mov_b32 s62, 2
	s_add_i32 s63, s63, 2
	s_mov_b32 s74, 0
	v_mov_b32_e32 v208, 0xf149f2ca
	v_mov_b32_e32 v209, 0
	s_movk_i32 s75, 0xc000
	v_mov_b64_e32 v[106:107], v[58:59]
	v_mov_b64_e32 v[104:105], v[56:57]
	v_mov_b64_e32 v[102:103], v[54:55]
	v_mov_b64_e32 v[100:101], v[52:53]
	v_mov_b64_e32 v[98:99], v[50:51]
	v_mov_b64_e32 v[96:97], v[48:49]
	v_mov_b64_e32 v[94:95], v[46:47]
	v_mov_b64_e32 v[122:123], v[58:59]
	v_mov_b64_e32 v[120:121], v[56:57]
	v_mov_b64_e32 v[118:119], v[54:55]
	v_mov_b64_e32 v[116:117], v[52:53]
	v_mov_b64_e32 v[114:115], v[50:51]
	v_mov_b64_e32 v[112:113], v[48:49]
	v_mov_b64_e32 v[110:111], v[46:47]
	v_mov_b64_e32 v[138:139], v[58:59]
	v_mov_b64_e32 v[136:137], v[56:57]
	v_mov_b64_e32 v[134:135], v[54:55]
	v_mov_b64_e32 v[132:133], v[52:53]
	v_mov_b64_e32 v[130:131], v[50:51]
	v_mov_b64_e32 v[128:129], v[48:49]
	v_mov_b64_e32 v[126:127], v[46:47]
	v_mov_b64_e32 v[154:155], v[58:59]
	v_mov_b64_e32 v[152:153], v[56:57]
	v_mov_b64_e32 v[150:151], v[54:55]
	v_mov_b64_e32 v[148:149], v[52:53]
	v_mov_b64_e32 v[146:147], v[50:51]
	v_mov_b64_e32 v[144:145], v[48:49]
	v_mov_b64_e32 v[142:143], v[46:47]
	v_mov_b64_e32 v[74:75], v[58:59]
	v_mov_b64_e32 v[72:73], v[56:57]
	v_mov_b64_e32 v[70:71], v[54:55]
	v_mov_b64_e32 v[68:69], v[52:53]
	v_mov_b64_e32 v[66:67], v[50:51]
	v_mov_b64_e32 v[64:65], v[48:49]
	v_mov_b64_e32 v[62:63], v[46:47]
	v_mov_b64_e32 v[90:91], v[58:59]
	v_mov_b64_e32 v[88:89], v[56:57]
	v_mov_b64_e32 v[86:87], v[54:55]
	v_mov_b64_e32 v[84:85], v[52:53]
	v_mov_b64_e32 v[82:83], v[50:51]
	v_mov_b64_e32 v[80:81], v[48:49]
	v_mov_b64_e32 v[78:79], v[46:47]
	v_and_b32_e32 v212, 0x1c0, v0
	v_lshlrev_b32_e32 v212, 6, v212
	v_and_b32_e32 v213, 63, v0
	v_lshlrev_b32_e32 v213, 2, v213
	v_add_u32_e32 v212, v212, v213
	v_add_u32_e32 v212, 0x1c000, v212
	ds_write_b32 v212, v234 offset:0
	ds_write_b32 v212, v235 offset:256
	ds_write_b32 v212, v236 offset:512
	ds_write_b32 v212, v237 offset:768
	ds_write_b32 v212, v238 offset:1024
	ds_write_b32 v212, v239 offset:1280
	ds_write_b32 v212, v240 offset:1536
	ds_write_b32 v212, v241 offset:1792
	ds_write_b32 v212, v242 offset:2048
	ds_write_b32 v212, v243 offset:2304
	ds_write_b32 v212, v226 offset:2560
	ds_write_b32 v212, v227 offset:2816
	ds_write_b32 v212, v246 offset:3072
	ds_write_b32 v212, v247 offset:3328
	ds_write_b32 v212, v245 offset:3584
	ds_write_b32 v212, v248 offset:3840
	s_waitcnt lgkmcnt(0)
	s_bitset0_b32 s101, 31
	s_bitset0_b32 s101, 30
	s_and_b32 s12, s101, 0x3fffffff
	s_cmp_ge_u32 s12, 168
	s_cbranch_scc1 .Lcn_ldum_n0sa
	s_and_b32 s12, s101, 0x3fffffff
	s_mul_i32 s13, s12, 0x2493
	s_lshr_b32 s13, s13, 16
	s_mul_i32 s65, s13, 7
	s_sub_u32 s65, s12, s65
	s_lshl_b32 s65, s65, 8
	s_lshr_b32 s66, s100, 3
	s_add_u32 s65, s65, s66
	s_and_b32 s12, s100, 7
	s_cmp_ge_u32 s13, 16
	s_cbranch_scc1 .Lcn_dn_n0sas
	s_lshr_b32 s66, s65, 4
	s_mul_i32 s66, s66, 0x2493
	s_lshr_b32 s66, s66, 16
	s_mul_i32 s0, s66, 0x70
	s_sub_u32 s0, s65, s0
	s_lshr_b32 s65, s12, 1
	s_lshl_b32 s66, s66, 2
	s_add_u32 s66, s66, s65
	s_and_b32 s12, s12, 1
	s_lshl_b32 s0, s0, 1
	s_add_u32 s0, s0, s12
	s_and_b32 s65, s13, 1
	s_lshr_b32 s13, s13, 1
	s_mul_i32 s12, s13, 0x3800000
	s_mul_i32 s13, s66, 0xe0000
	s_add_u32 s12, s12, s13
	s_lshl_b32 s13, s0, 7
	s_add_u32 s12, s12, s13
	v_readlane_b32 s32, v255, 46
	v_readlane_b32 s33, v255, 47
	s_cmp_eq_u32 s65, 0
	s_cselect_b32 s32, s98, s32
	s_cselect_b32 s33, s99, s33
	s_add_u32 s32, s32, s12
	s_addc_u32 s33, s33, 0
	s_movk_i32 s1, 0x7000
	s_branch .Lcn_dd_n0sas
.Lcn_dn_n0sas:
	s_sub_u32 s13, s13, 16
	s_lshr_b32 s66, s65, 5
	s_and_b32 s0, s65, 31
	s_lshr_b32 s65, s12, 1
	s_lshl_b32 s66, s66, 2
	s_add_u32 s66, s66, s65
	s_and_b32 s12, s12, 1
	s_lshl_b32 s0, s0, 1
	s_add_u32 s0, s0, s12
	s_mul_i32 s12, s13, 0x3800000
	s_lshl_b32 s13, s66, 18
	s_add_u32 s12, s12, s13
	s_lshl_b32 s13, s0, 7
	s_add_u32 s12, s12, s13
	v_readlane_b32 s32, v255, 48
	v_readlane_b32 s33, v255, 49
	s_add_u32 s32, s32, s12
	s_addc_u32 s33, s33, 0
	s_movk_i32 s1, 0x2000
.Lcn_dd_n0sas:
	s_and_b32 s25, s101, 0x3fffffff
	s_bitset1_b32 s25, 31
	s_add_u32 s101, s101, 1
	s_branch .Lcn_lgo_n0sa
.Lcn_ldum_n0sa:
	v_readlane_b32 s32, v255, 52
	v_readlane_b32 s33, v255, 53
	s_add_u32 s32, s32, 0x500000
	s_addc_u32 s33, s33, 0
	s_movk_i32 s1, 0x2000
	s_mov_b32 s25, 0
.Lcn_lgo_n0sa:
	v_and_b32_e32 v224, 63, v0
	v_and_b32_e32 v253, 7, v224
	v_lshrrev_b32_e32 v224, 3, v224
	v_lshlrev_b32_e32 v224, 2, v224
	v_lshlrev_b32_e32 v225, 4, v253
	v_lshlrev_b32_e32 v253, 2, v253
	v_mad_u32_u24 v254, v224, s1, v225
	global_load_dwordx4 v[212:215], v254, s[32:33] nt
	s_add_u32 s32, s32, s1
	s_addc_u32 s33, s33, 0
	global_load_dwordx4 v[216:219], v254, s[32:33] nt
	s_add_u32 s32, s32, s1
	s_addc_u32 s33, s33, 0
	global_load_dwordx4 v[220:223], v254, s[32:33] nt
	s_add_u32 s32, s32, s1
	s_addc_u32 s33, s33, 0
	global_load_dwordx2 v[224:225], v254, s[32:33] offset:0 nt
	global_load_dword v253, v254, s[32:33] offset:8 nt
	global_load_dword v254, v254, s[32:33] offset:12 nt
	s_and_b32 s12, s101, 0x3fffffff
	s_cmp_ge_u32 s12, 168
	s_cbranch_scc1 .Lcn_ldum_n0sb
	s_and_b32 s12, s101, 0x3fffffff
	s_mul_i32 s13, s12, 0x2493
	s_lshr_b32 s13, s13, 16
	s_mul_i32 s65, s13, 7
	s_sub_u32 s65, s12, s65
	s_lshl_b32 s65, s65, 8
	s_lshr_b32 s66, s100, 3
	s_add_u32 s65, s65, s66
	s_and_b32 s12, s100, 7
	s_cmp_ge_u32 s13, 16
	s_cbranch_scc1 .Lcn_dn_n0sbs
	s_lshr_b32 s66, s65, 4
	s_mul_i32 s66, s66, 0x2493
	s_lshr_b32 s66, s66, 16
	s_mul_i32 s0, s66, 0x70
	s_sub_u32 s0, s65, s0
	s_lshr_b32 s65, s12, 1
	s_lshl_b32 s66, s66, 2
	s_add_u32 s66, s66, s65
	s_and_b32 s12, s12, 1
	s_lshl_b32 s0, s0, 1
	s_add_u32 s0, s0, s12
	s_and_b32 s65, s13, 1
	s_lshr_b32 s13, s13, 1
	s_mul_i32 s12, s13, 0x3800000
	s_mul_i32 s13, s66, 0xe0000
	s_add_u32 s12, s12, s13
	s_lshl_b32 s13, s0, 7
	s_add_u32 s12, s12, s13
	v_readlane_b32 s32, v255, 46
	v_readlane_b32 s33, v255, 47
	s_cmp_eq_u32 s65, 0
	s_cselect_b32 s32, s98, s32
	s_cselect_b32 s33, s99, s33
	s_add_u32 s32, s32, s12
	s_addc_u32 s33, s33, 0
	s_movk_i32 s1, 0x7000
	s_branch .Lcn_dd_n0sbs

; __device__ __forceinline__ void witem_load(const WItem& w, f32x4 (&v)[16]) {
;     if (!w.valid) return;
; #pragma unroll
;     for (int i = 0; i < 16; ++i) v[i] = *(const f32x4*)(w.src + (size_t)i * w.N);
; }
; __device__ __forceinline__ void nsa_unit(const Args& a, LAS unsigned char* lds, int b, int kvh, int qb) {
;     ...
;     for (int it = 0; it <= nTot; ++it) {
;         if (it + 1 < nTot) asm volatile("s_waitcnt vmcnt(4) lgkmcnt(0)\n\ts_barrier" ::: "memory"); else asm volatile("s_waitcnt vmcnt(0) lgkmcnt(0)\n\ts_barrier" ::: "memory");
.Lcn_dd_n0sbs:
	s_and_b32 s67, s101, 0x3fffffff
	s_bitset1_b32 s67, 31
	s_add_u32 s101, s101, 1
	s_branch .Lcn_lgo_n0sb
.Lcn_ldum_n0sb:
	v_readlane_b32 s32, v255, 52
	v_readlane_b32 s33, v255, 53
	s_add_u32 s32, s32, 0x500000
	s_addc_u32 s33, s33, 0
	s_movk_i32 s1, 0x2000
	s_mov_b32 s67, 0
.Lcn_lgo_n0sb:
	v_and_b32_e32 v246, 63, v0
	v_and_b32_e32 v245, 7, v246
	v_lshrrev_b32_e32 v246, 3, v246
	v_lshlrev_b32_e32 v246, 2, v246
	v_lshlrev_b32_e32 v247, 4, v245
	v_lshlrev_b32_e32 v245, 2, v245
	v_mad_u32_u24 v248, v246, s1, v247
	global_load_dwordx4 v[234:237], v248, s[32:33] nt
	s_add_u32 s32, s32, s1
	s_addc_u32 s33, s33, 0
	global_load_dwordx4 v[238:241], v248, s[32:33] nt
	s_add_u32 s32, s32, s1
	s_addc_u32 s33, s33, 0
	global_load_dwordx2 v[242:243], v248, s[32:33] offset:0 nt
	global_load_dwordx2 v[226:227], v248, s[32:33] offset:8 nt
	s_add_u32 s32, s32, s1
	s_addc_u32 s33, s33, 0
	global_load_dwordx2 v[246:247], v248, s[32:33] offset:0 nt
	global_load_dword v245, v248, s[32:33] offset:8 nt
	global_load_dword v248, v248, s[32:33] offset:12 nt
	s_branch .LBB0_897
.LBB0_896:
	s_bitcmp1_b32 s101, 31
	s_cbranch_scc1 .Lcn_lB_n0
	s_bitcmp1_b32 s101, 30
	s_cbranch_scc1 .Lcn_wf_n0A
	s_add_i32 s12, s74, 2
	s_cmp_gt_i32 s12, s15
	s_cbranch_scc1 .Lcn_w0_n0A0
	s_waitcnt vmcnt(11)
	s_branch .Lcn_wd_n0A
.Lcn_w0_n0A0:
	s_cmp_gt_i32 s74, s15
	s_cbranch_scc1 .Lcn_w1_n0A0
	s_waitcnt vmcnt(7)
	s_branch .Lcn_wd_n0A
.Lcn_w1_n0A0:
	s_waitcnt vmcnt(0)
	s_branch .Lcn_wd_n0A
.Lcn_wf_n0A:
	s_add_i32 s12, s74, 2
	s_cmp_gt_i32 s12, s15
	s_cbranch_scc1 .Lcn_w0_n0A1
	s_waitcnt vmcnt(15)
	s_branch .Lcn_wd_n0A
.Lcn_w0_n0A1:
	s_cmp_gt_i32 s74, s15
	s_cbranch_scc1 .Lcn_w1_n0A1
	s_waitcnt vmcnt(11)
	s_branch .Lcn_wd_n0A

; __device__ __forceinline__ unsigned pk4_fp8(float a, float b, float c, float d) { int p = __builtin_amdgcn_cvt_pk_fp8_f32(a, b, 0, false); p = __builtin_amdgcn_cvt_pk_fp8_f32(c, d, p, true); return (unsigned)p; }
; __device__ __forceinline__ void witem_store(const WItem& w, const f32x4 (&v)[16]) {
;     if (!w.valid) return;
;     if (w.f8) {
; #pragma unroll
;         for (int j = 0; j < 4; ++j) { u32x4 o; const float sc = w.scale;
;             o.x = pk4_fp8(v[0][j] * sc, v[1][j] * sc, v[2][j] * sc, v[3][j] * sc); o.y = pk4_fp8(v[4][j] * sc, v[5][j] * sc, v[6][j] * sc, v[7][j] * sc);
;             o.z = pk4_fp8(v[8][j] * sc, v[9][j] * sc, v[10][j] * sc, v[11][j] * sc); o.w = pk4_fp8(v[12][j] * sc, v[13][j] * sc, v[14][j] * sc, v[15][j] * sc);
;             *(u32x4*)(w.dst + (size_t)witem_row(w.kind, w.n + j) * w.K + w.k0) = o; }
; __device__ __forceinline__ void p0_weights(const Args& a, LAS unsigned char* lds) {
;     ...
;         else if ((r -= I_FD) < 16 * I_MG) { const int up = r / (8 * I_MG); r -= up * 8 * I_MG; const int e = r / I_MG; r -= e * I_MG; W = a.in[up ? I_MWU : I_MWG] + (size_t)e * D * DFE; w.K = D; w.N = DFE;
;             w.dst = a.ws + WS_MGU_T + (size_t)e * 2 * DFE * D * (MOE_FP8 ? 1 : 2); w.kind = 2 + up; w.f8 = MOE_FP8; w.scale = F8_WGU; }
;         else { r -= 16 * I_MG; const int e = r / I_MD; r -= e * I_MD; W = a.in[I_MWD] + (size_t)e * DFE * D; w.K = DFE; w.N = D; w.dst = a.ws + WS_MD_T + (size_t)e * D * DFE * (MOE_FP8 ? 1 : 2); w.f8 = MOE_FP8; w.scale = F8_WD; }
;         const int nblk = (w.N + 31) >> 5, kb = r / nblk, nb = r - kb * nblk;
;         w.k0 = 128 * kb + 16 * (lane >> 3); w.n = 32 * nb + 4 * (lane & 7); w.valid = w.n < w.N; w.src = W + (size_t)w.k0 * w.N + w.n;
.Lcn_wd_n0A:
	s_bitset0_b32 s101, 30
	s_bitcmp1_b32 s25, 31
	s_cbranch_scc0 .Lcn_snone_n0Al
	s_and_b32 s12, s25, 0x3fffffff
	s_mul_i32 s13, s12, 0x2493
	s_lshr_b32 s13, s13, 16
	s_mul_i32 s65, s13, 7
	s_sub_u32 s65, s12, s65
	s_lshl_b32 s65, s65, 8
	s_lshr_b32 s66, s100, 3
	s_add_u32 s65, s65, s66
	s_and_b32 s12, s100, 7
	s_cmp_ge_u32 s13, 16
	s_cbranch_scc1 .Lcn_dn_n0Ald
	s_lshr_b32 s66, s65, 4
	s_mul_i32 s66, s66, 0x2493
	s_lshr_b32 s66, s66, 16
	s_mul_i32 s0, s66, 0x70
	s_sub_u32 s0, s65, s0
	s_lshr_b32 s65, s12, 1
	s_lshl_b32 s66, s66, 2
	s_add_u32 s66, s66, s65
	s_and_b32 s12, s12, 1
	s_lshl_b32 s0, s0, 1
	s_add_u32 s0, s0, s12
	s_and_b32 s65, s13, 1
	s_lshr_b32 s13, s13, 1
	s_mul_i32 s12, s13, 0x1c00000
	s_add_u32 s12, s12, 0x4a000000
	s_lshr_b32 s13, s0, 2
	s_lshl_b32 s13, s13, 8
	s_lshl_b32 s65, s65, 7
	s_add_u32 s13, s13, s65
	s_and_b32 s65, s0, 3
	s_lshl_b32 s65, s65, 5
	s_add_u32 s13, s13, s65
	s_lshl_b32 s13, s13, 11
	s_add_u32 s12, s12, s13
	s_lshl_b32 s13, s66, 5
	s_add_u32 s12, s12, s13
	v_readlane_b32 s32, v255, 52
	v_readlane_b32 s33, v255, 53
	s_add_u32 s32, s32, s12
	s_addc_u32 s33, s33, 0
	s_movk_i32 s1, 0x800
	s_mov_b32 s0, 0x42000000
	s_branch .Lcn_dd_n0Ald
.Lcn_dn_n0Ald:
	s_sub_u32 s13, s13, 16
	s_lshr_b32 s66, s65, 5
	s_and_b32 s0, s65, 31
	s_lshr_b32 s65, s12, 1
	s_lshl_b32 s66, s66, 2
	s_add_u32 s66, s66, s65
	s_and_b32 s12, s12, 1
	s_lshl_b32 s0, s0, 1
	s_add_u32 s0, s0, s12
	s_mul_i32 s12, s13, 0xe00000
	s_add_u32 s12, s12, 0x66000000
	s_mul_i32 s13, s0, 0x38000
	s_add_u32 s12, s12, s13
	s_lshl_b32 s13, s66, 5
	s_add_u32 s12, s12, s13
	v_readlane_b32 s32, v255, 52
	v_readlane_b32 s33, v255, 53
	s_add_u32 s32, s32, s12
	s_addc_u32 s33, s33, 0
	s_movk_i32 s1, 0x1c00
	s_mov_b32 s0, 0x43000000
.Lcn_dd_n0Ald:
	s_mov_b32 s25, 0
	s_bitset1_b32 s101, 30
	v_mul_f32_e32 v212, s0, v212
	v_mul_f32_e32 v213, s0, v213
	v_mul_f32_e32 v214, s0, v214
	v_mul_f32_e32 v215, s0, v215
	v_mul_f32_e32 v216, s0, v216
	v_mul_f32_e32 v217, s0, v217
	v_mul_f32_e32 v218, s0, v218
	v_mul_f32_e32 v219, s0, v219
	v_mul_f32_e32 v220, s0, v220
	v_mul_f32_e32 v221, s0, v221
	v_mul_f32_e32 v222, s0, v222
	v_mul_f32_e32 v223, s0, v223
	v_mul_f32_e32 v224, s0, v224
	v_mul_f32_e32 v225, s0, v225
	v_mul_f32_e32 v253, s0, v253
	v_mul_f32_e32 v254, s0, v254
	v_cvt_pk_fp8_f32 v212, v212, v216
	v_cvt_pk_fp8_f32 v213, v213, v217
	v_cvt_pk_fp8_f32 v214, v214, v218
	v_cvt_pk_fp8_f32 v215, v215, v219
	v_cvt_pk_fp8_f32 v212, v220, v224 op_sel:[0,0,1]
	v_cvt_pk_fp8_f32 v213, v221, v225 op_sel:[0,0,1]
	v_cvt_pk_fp8_f32 v214, v222, v253 op_sel:[0,0,1]
	v_cvt_pk_fp8_f32 v215, v223, v254 op_sel:[0,0,1]
	v_and_b32_e32 v216, 63, v0
	v_and_b32_e32 v218, 7, v216
	v_lshrrev_b32_e32 v216, 3, v216
	v_lshlrev_b32_e32 v216, 2, v216
	v_lshlrev_b32_e32 v217, 4, v218
	v_lshlrev_b32_e32 v218, 2, v218
	v_mad_u32_u24 v217, v218, s1, v216
	global_store_dword v217, v212, s[32:33] nt
	v_add_u32_e32 v216, s1, v217
	global_store_dword v216, v213, s[32:33] nt
	v_add_u32_e32 v218, s1, v216
	global_store_dword v218, v214, s[32:33] nt
	v_add_u32_e32 v219, s1, v218
	global_store_dword v219, v215, s[32:33] nt
.Lcn_snone_n0Al:
	s_mov_b32 s25, 0
	s_add_i32 s12, s74, 1
	s_cmp_gt_i32 s12, s15
	s_cbranch_scc1 .Lcn_lskip_n0Al
	s_and_b32 s12, s101, 0x3fffffff
	s_cmp_ge_u32 s12, 168
	s_cbranch_scc1 .Lcn_ldum_n0Al
	s_and_b32 s12, s101, 0x3fffffff
	s_mul_i32 s13, s12, 0x2493
	s_lshr_b32 s13, s13, 16
	s_mul_i32 s65, s13, 7
	s_sub_u32 s65, s12, s65
	s_lshl_b32 s65, s65, 8
	s_lshr_b32 s66, s100, 3
	s_add_u32 s65, s65, s66
	s_and_b32 s12, s100, 7
	s_cmp_ge_u32 s13, 16
	s_cbranch_scc1 .Lcn_dn_n0Als
	s_lshr_b32 s66, s65, 4
	s_mul_i32 s66, s66, 0x2493
	s_lshr_b32 s66, s66, 16
	s_mul_i32 s0, s66, 0x70
	s_sub_u32 s0, s65, s0
	s_lshr_b32 s65, s12, 1
	s_lshl_b32 s66, s66, 2
	s_add_u32 s66, s66, s65
	s_and_b32 s12, s12, 1
	s_lshl_b32 s0, s0, 1
	s_add_u32 s0, s0, s12
	s_and_b32 s65, s13, 1
	s_lshr_b32 s13, s13, 1
	s_mul_i32 s12, s13, 0x3800000
	s_mul_i32 s13, s66, 0xe0000
	s_add_u32 s12, s12, s13
	s_lshl_b32 s13, s0, 7
	s_add_u32 s12, s12, s13
	v_readlane_b32 s32, v255, 46
	v_readlane_b32 s33, v255, 47
	s_cmp_eq_u32 s65, 0
	s_cselect_b32 s32, s98, s32
	s_cselect_b32 s33, s99, s33
	s_add_u32 s32, s32, s12
	s_addc_u32 s33, s33, 0
	s_movk_i32 s1, 0x7000
	s_branch .Lcn_dd_n0Als

; __device__ __forceinline__ void witem_load(const WItem& w, f32x4 (&v)[16]) {
;     if (!w.valid) return;
; #pragma unroll
;     for (int i = 0; i < 16; ++i) v[i] = *(const f32x4*)(w.src + (size_t)i * w.N);
; }
; __device__ __forceinline__ void nsa_unit(const Args& a, LAS unsigned char* lds, int b, int kvh, int qb) {
;     ...
;     for (int it = 0; it <= nTot; ++it) {
;         if (it + 1 < nTot) asm volatile("s_waitcnt vmcnt(4) lgkmcnt(0)\n\ts_barrier" ::: "memory"); else asm volatile("s_waitcnt vmcnt(0) lgkmcnt(0)\n\ts_barrier" ::: "memory");
.Lcn_lgo_n0Al:
	v_and_b32_e32 v224, 63, v0
	v_and_b32_e32 v253, 7, v224
	v_lshrrev_b32_e32 v224, 3, v224
	v_lshlrev_b32_e32 v224, 2, v224
	v_lshlrev_b32_e32 v225, 4, v253
	v_lshlrev_b32_e32 v253, 2, v253
	v_mad_u32_u24 v254, v224, s1, v225
	global_load_dwordx4 v[212:215], v254, s[32:33] nt
	s_add_u32 s32, s32, s1
	s_addc_u32 s33, s33, 0
	global_load_dwordx4 v[216:219], v254, s[32:33] nt
	s_add_u32 s32, s32, s1
	s_addc_u32 s33, s33, 0
	global_load_dwordx4 v[220:223], v254, s[32:33] nt
	s_add_u32 s32, s32, s1
	s_addc_u32 s33, s33, 0
	global_load_dwordx2 v[224:225], v254, s[32:33] offset:0 nt
	global_load_dword v253, v254, s[32:33] offset:8 nt
	global_load_dword v254, v254, s[32:33] offset:12 nt
.Lcn_lskip_n0Al:
	s_bitset1_b32 s101, 31
	s_branch .Lcn_ld_n0
.Lcn_lB_n0:
	s_bitcmp1_b32 s101, 30
	s_cbranch_scc1 .Lcn_wf_n0B
	s_add_i32 s12, s74, 2
	s_cmp_gt_i32 s12, s15
	s_cbranch_scc1 .Lcn_w0_n0B0
	s_waitcnt vmcnt(10)
	s_branch .Lcn_wd_n0B
.Lcn_w0_n0B0:
	s_cmp_gt_i32 s74, s15
	s_cbranch_scc1 .Lcn_w1_n0B0
	s_waitcnt vmcnt(6)
	s_branch .Lcn_wd_n0B

; __device__ __forceinline__ void nsa_unit(const Args& a, LAS unsigned char* lds, int b, int kvh, int qb) {
;     ...
;     for (int it = 0; it <= nTot; ++it) {
;         if (it + 1 < nTot) asm volatile("s_waitcnt vmcnt(4) lgkmcnt(0)\n\ts_barrier" ::: "memory"); else asm volatile("s_waitcnt vmcnt(0) lgkmcnt(0)\n\ts_barrier" ::: "memory");
.Lcn_wf_n0B:
	s_add_i32 s12, s74, 2
	s_cmp_gt_i32 s12, s15
	s_cbranch_scc1 .Lcn_w0_n0B1
	s_waitcnt vmcnt(14)
	s_branch .Lcn_wd_n0B
.Lcn_w0_n0B1:
	s_cmp_gt_i32 s74, s15
	s_cbranch_scc1 .Lcn_w1_n0B1
	s_waitcnt vmcnt(10)
	s_branch .Lcn_wd_n0B

; __device__ __forceinline__ void p0_weights(const Args& a, LAS unsigned char* lds) {
;     ...
;         else if ((r -= I_FD) < 16 * I_MG) { const int up = r / (8 * I_MG); r -= up * 8 * I_MG; const int e = r / I_MG; r -= e * I_MG; W = a.in[up ? I_MWU : I_MWG] + (size_t)e * D * DFE; w.K = D; w.N = DFE;
;             w.dst = a.ws + WS_MGU_T + (size_t)e * 2 * DFE * D * (MOE_FP8 ? 1 : 2); w.kind = 2 + up; w.f8 = MOE_FP8; w.scale = F8_WGU; }
;         else { r -= 16 * I_MG; const int e = r / I_MD; r -= e * I_MD; W = a.in[I_MWD] + (size_t)e * DFE * D; w.K = DFE; w.N = D; w.dst = a.ws + WS_MD_T + (size_t)e * D * DFE * (MOE_FP8 ? 1 : 2); w.f8 = MOE_FP8; w.scale = F8_WD; }
;         const int nblk = (w.N + 31) >> 5, kb = r / nblk, nb = r - kb * nblk;
;         w.k0 = 128 * kb + 16 * (lane >> 3); w.n = 32 * nb + 4 * (lane & 7); w.valid = w.n < w.N; w.src = W + (size_t)w.k0 * w.N + w.n;
.Lcn_wd_n0B:
	s_bitset0_b32 s101, 30
	s_bitcmp1_b32 s67, 31
	s_cbranch_scc0 .Lcn_snone_n0Bl
	s_and_b32 s12, s67, 0x3fffffff
	s_mul_i32 s13, s12, 0x2493
	s_lshr_b32 s13, s13, 16
	s_mul_i32 s65, s13, 7
	s_sub_u32 s65, s12, s65
	s_lshl_b32 s65, s65, 8
	s_lshr_b32 s66, s100, 3
	s_add_u32 s65, s65, s66
	s_and_b32 s12, s100, 7
	s_cmp_ge_u32 s13, 16
	s_cbranch_scc1 .Lcn_dn_n0Bld
	s_lshr_b32 s66, s65, 4
	s_mul_i32 s66, s66, 0x2493
	s_lshr_b32 s66, s66, 16
	s_mul_i32 s0, s66, 0x70
	s_sub_u32 s0, s65, s0
	s_lshr_b32 s65, s12, 1
	s_lshl_b32 s66, s66, 2
	s_add_u32 s66, s66, s65
	s_and_b32 s12, s12, 1
	s_lshl_b32 s0, s0, 1
	s_add_u32 s0, s0, s12
	s_and_b32 s65, s13, 1
	s_lshr_b32 s13, s13, 1
	s_mul_i32 s12, s13, 0x1c00000
	s_add_u32 s12, s12, 0x4a000000
	s_lshr_b32 s13, s0, 2
	s_lshl_b32 s13, s13, 8
	s_lshl_b32 s65, s65, 7
	s_add_u32 s13, s13, s65
	s_and_b32 s65, s0, 3
	s_lshl_b32 s65, s65, 5
	s_add_u32 s13, s13, s65
	s_lshl_b32 s13, s13, 11
	s_add_u32 s12, s12, s13
	s_lshl_b32 s13, s66, 5
	s_add_u32 s12, s12, s13
	v_readlane_b32 s32, v255, 52
	v_readlane_b32 s33, v255, 53
	s_add_u32 s32, s32, s12
	s_addc_u32 s33, s33, 0
	s_movk_i32 s1, 0x800
	s_mov_b32 s0, 0x42000000
	s_branch .Lcn_dd_n0Bld

; __device__ __forceinline__ unsigned pk4_fp8(float a, float b, float c, float d) { int p = __builtin_amdgcn_cvt_pk_fp8_f32(a, b, 0, false); p = __builtin_amdgcn_cvt_pk_fp8_f32(c, d, p, true); return (unsigned)p; }
; __device__ __forceinline__ void witem_store(const WItem& w, const f32x4 (&v)[16]) {
;     if (!w.valid) return;
;     if (w.f8) {
; #pragma unroll
;         for (int j = 0; j < 4; ++j) { u32x4 o; const float sc = w.scale;
;             o.x = pk4_fp8(v[0][j] * sc, v[1][j] * sc, v[2][j] * sc, v[3][j] * sc); o.y = pk4_fp8(v[4][j] * sc, v[5][j] * sc, v[6][j] * sc, v[7][j] * sc);
;             o.z = pk4_fp8(v[8][j] * sc, v[9][j] * sc, v[10][j] * sc, v[11][j] * sc); o.w = pk4_fp8(v[12][j] * sc, v[13][j] * sc, v[14][j] * sc, v[15][j] * sc);
;             *(u32x4*)(w.dst + (size_t)witem_row(w.kind, w.n + j) * w.K + w.k0) = o; }
; __device__ __forceinline__ void p0_weights(const Args& a, LAS unsigned char* lds) {
;     ...
;         else if ((r -= I_FD) < 16 * I_MG) { const int up = r / (8 * I_MG); r -= up * 8 * I_MG; const int e = r / I_MG; r -= e * I_MG; W = a.in[up ? I_MWU : I_MWG] + (size_t)e * D * DFE; w.K = D; w.N = DFE;
;             w.dst = a.ws + WS_MGU_T + (size_t)e * 2 * DFE * D * (MOE_FP8 ? 1 : 2); w.kind = 2 + up; w.f8 = MOE_FP8; w.scale = F8_WGU; }
;         else { r -= 16 * I_MG; const int e = r / I_MD; r -= e * I_MD; W = a.in[I_MWD] + (size_t)e * DFE * D; w.K = DFE; w.N = D; w.dst = a.ws + WS_MD_T + (size_t)e * D * DFE * (MOE_FP8 ? 1 : 2); w.f8 = MOE_FP8; w.scale = F8_WD; }
;         const int nblk = (w.N + 31) >> 5, kb = r / nblk, nb = r - kb * nblk;
;         w.k0 = 128 * kb + 16 * (lane >> 3); w.n = 32 * nb + 4 * (lane & 7); w.valid = w.n < w.N; w.src = W + (size_t)w.k0 * w.N + w.n;
.Lcn_dd_n0Bld:
	s_mov_b32 s67, 0
	s_bitset1_b32 s101, 30
	v_mul_f32_e32 v234, s0, v234
	v_mul_f32_e32 v235, s0, v235
	v_mul_f32_e32 v236, s0, v236
	v_mul_f32_e32 v237, s0, v237
	v_mul_f32_e32 v238, s0, v238
	v_mul_f32_e32 v239, s0, v239
	v_mul_f32_e32 v240, s0, v240
	v_mul_f32_e32 v241, s0, v241
	v_mul_f32_e32 v242, s0, v242
	v_mul_f32_e32 v243, s0, v243
	v_mul_f32_e32 v226, s0, v226
	v_mul_f32_e32 v227, s0, v227
	v_mul_f32_e32 v246, s0, v246
	v_mul_f32_e32 v247, s0, v247
	v_mul_f32_e32 v245, s0, v245
	v_mul_f32_e32 v248, s0, v248
	v_cvt_pk_fp8_f32 v234, v234, v238
	v_cvt_pk_fp8_f32 v235, v235, v239
	v_cvt_pk_fp8_f32 v236, v236, v240
	v_cvt_pk_fp8_f32 v237, v237, v241
	v_cvt_pk_fp8_f32 v234, v242, v246 op_sel:[0,0,1]
	v_cvt_pk_fp8_f32 v235, v243, v247 op_sel:[0,0,1]
	v_cvt_pk_fp8_f32 v236, v226, v245 op_sel:[0,0,1]
	v_cvt_pk_fp8_f32 v237, v227, v248 op_sel:[0,0,1]
	v_and_b32_e32 v238, 63, v0
	v_and_b32_e32 v240, 7, v238
	v_lshrrev_b32_e32 v238, 3, v238
	v_lshlrev_b32_e32 v238, 2, v238
	v_lshlrev_b32_e32 v239, 4, v240
	v_lshlrev_b32_e32 v240, 2, v240
	v_mad_u32_u24 v239, v240, s1, v238
	global_store_dword v239, v234, s[32:33] nt
	v_add_u32_e32 v238, s1, v239
	global_store_dword v238, v235, s[32:33] nt
	v_add_u32_e32 v240, s1, v238
	global_store_dword v240, v236, s[32:33] nt
	v_add_u32_e32 v241, s1, v240
	global_store_dword v241, v237, s[32:33] nt
.Lcn_snone_n0Bl:
	s_mov_b32 s67, 0
	s_add_i32 s12, s74, 1
	s_cmp_gt_i32 s12, s15
	s_cbranch_scc1 .Lcn_lskip_n0Bl
	s_and_b32 s12, s101, 0x3fffffff
	s_cmp_ge_u32 s12, 168
	s_cbranch_scc1 .Lcn_ldum_n0Bl
	s_and_b32 s12, s101, 0x3fffffff
	s_mul_i32 s13, s12, 0x2493
	s_lshr_b32 s13, s13, 16
	s_mul_i32 s65, s13, 7
	s_sub_u32 s65, s12, s65
	s_lshl_b32 s65, s65, 8
	s_lshr_b32 s66, s100, 3
	s_add_u32 s65, s65, s66
	s_and_b32 s12, s100, 7
	s_cmp_ge_u32 s13, 16
	s_cbranch_scc1 .Lcn_dn_n0Bls
	s_lshr_b32 s66, s65, 4
	s_mul_i32 s66, s66, 0x2493
	s_lshr_b32 s66, s66, 16
	s_mul_i32 s0, s66, 0x70
	s_sub_u32 s0, s65, s0
	s_lshr_b32 s65, s12, 1
	s_lshl_b32 s66, s66, 2
	s_add_u32 s66, s66, s65
	s_and_b32 s12, s12, 1
	s_lshl_b32 s0, s0, 1
	s_add_u32 s0, s0, s12
	s_and_b32 s65, s13, 1
	s_lshr_b32 s13, s13, 1
	s_mul_i32 s12, s13, 0x3800000
	s_mul_i32 s13, s66, 0xe0000
	s_add_u32 s12, s12, s13
	s_lshl_b32 s13, s0, 7
	s_add_u32 s12, s12, s13
	v_readlane_b32 s32, v255, 46
	v_readlane_b32 s33, v255, 47
	s_cmp_eq_u32 s65, 0
	s_cselect_b32 s32, s98, s32
	s_cselect_b32 s33, s99, s33
	s_add_u32 s32, s32, s12
	s_addc_u32 s33, s33, 0
	s_movk_i32 s1, 0x7000
	s_branch .Lcn_dd_n0Bls

; __device__ __forceinline__ void witem_load(const WItem& w, f32x4 (&v)[16]) {
;     if (!w.valid) return;
; #pragma unroll
;     for (int i = 0; i < 16; ++i) v[i] = *(const f32x4*)(w.src + (size_t)i * w.N);
; }
.Lcn_lgo_n0Bl:
	v_and_b32_e32 v246, 63, v0
	v_and_b32_e32 v245, 7, v246
	v_lshrrev_b32_e32 v246, 3, v246
	v_lshlrev_b32_e32 v246, 2, v246
	v_lshlrev_b32_e32 v247, 4, v245
	v_lshlrev_b32_e32 v245, 2, v245
	v_mad_u32_u24 v248, v246, s1, v247
	global_load_dwordx4 v[234:237], v248, s[32:33] nt
	s_add_u32 s32, s32, s1
	s_addc_u32 s33, s33, 0
	global_load_dwordx4 v[238:241], v248, s[32:33] nt
	s_add_u32 s32, s32, s1
	s_addc_u32 s33, s33, 0
	global_load_dwordx2 v[242:243], v248, s[32:33] offset:0 nt
	global_load_dwordx2 v[226:227], v248, s[32:33] offset:8 nt
	s_add_u32 s32, s32, s1
	s_addc_u32 s33, s33, 0
	global_load_dwordx2 v[246:247], v248, s[32:33] offset:0 nt
	global_load_dword v245, v248, s[32:33] offset:8 nt
	global_load_dword v248, v248, s[32:33] offset:12 nt

; __device__ __forceinline__ void nsa_unit(const Args& a, LAS unsigned char* lds, int b, int kvh, int qb) {
;     ...
;     for (int it = 0; it <= nTot; ++it) {
;         if (it + 1 < nTot) asm volatile("s_waitcnt vmcnt(4) lgkmcnt(0)\n\ts_barrier" ::: "memory"); else asm volatile("s_waitcnt vmcnt(0) lgkmcnt(0)\n\ts_barrier" ::: "memory");
.LBB0_897:
	s_cmp_ge_i32 s74, s15
	s_mov_b64 s[0:1], -1
	s_cbranch_scc0 .LBB0_900
	s_waitcnt vmcnt(13) lgkmcnt(0)
	s_barrier
	s_cbranch_execz .LBB0_901

; __device__ __forceinline__ void nsa_unit(const Args& a, LAS unsigned char* lds, int b, int kvh, int qb) {
;     ...
;         asm volatile("s_waitcnt lgkmcnt(0)\n\ts_barrier" ::: "memory");
.LBB0_901:
	s_waitcnt vmcnt(17) lgkmcnt(0)
	s_barrier
	s_cmp_lg_u32 s74, 0
	s_cselect_b64 s[0:1], -1, 0
	s_cmp_eq_u32 s74, 0
	s_cbranch_scc1 .LBB0_912

; __device__ __forceinline__ void p0_weights(const Args& a, LAS unsigned char* lds) {
;     ...
;         else if ((r -= I_FD) < 16 * I_MG) { const int up = r / (8 * I_MG); r -= up * 8 * I_MG; const int e = r / I_MG; r -= e * I_MG; W = a.in[up ? I_MWU : I_MWG] + (size_t)e * D * DFE; w.K = D; w.N = DFE;
;             w.dst = a.ws + WS_MGU_T + (size_t)e * 2 * DFE * D * (MOE_FP8 ? 1 : 2); w.kind = 2 + up; w.f8 = MOE_FP8; w.scale = F8_WGU; }
;         else { r -= 16 * I_MG; const int e = r / I_MD; r -= e * I_MD; W = a.in[I_MWD] + (size_t)e * DFE * D; w.K = DFE; w.N = D; w.dst = a.ws + WS_MD_T + (size_t)e * D * DFE * (MOE_FP8 ? 1 : 2); w.f8 = MOE_FP8; w.scale = F8_WD; }
;         const int nblk = (w.N + 31) >> 5, kb = r / nblk, nb = r - kb * nblk;
;         w.k0 = 128 * kb + 16 * (lane >> 3); w.n = 32 * nb + 4 * (lane & 7); w.valid = w.n < w.N; w.src = W + (size_t)w.k0 * w.N + w.n;
.Lcn_exit_n0:
	s_or_b32 s12, s25, s67
	s_bitcmp1_b32 s12, 31
	s_cbranch_scc0 .Lcn_xnone_n0
	s_waitcnt vmcnt(0)
	s_bitset0_b32 s101, 30
	s_bitcmp1_b32 s25, 31
	s_cbranch_scc0 .Lcn_snone_n0xa
	s_and_b32 s12, s25, 0x3fffffff
	s_mul_i32 s13, s12, 0x2493
	s_lshr_b32 s13, s13, 16
	s_mul_i32 s65, s13, 7
	s_sub_u32 s65, s12, s65
	s_lshl_b32 s65, s65, 8
	s_lshr_b32 s66, s100, 3
	s_add_u32 s65, s65, s66
	s_and_b32 s12, s100, 7
	s_cmp_ge_u32 s13, 16
	s_cbranch_scc1 .Lcn_dn_n0xad
	s_lshr_b32 s66, s65, 4
	s_mul_i32 s66, s66, 0x2493
	s_lshr_b32 s66, s66, 16
	s_mul_i32 s0, s66, 0x70
	s_sub_u32 s0, s65, s0
	s_lshr_b32 s65, s12, 1
	s_lshl_b32 s66, s66, 2
	s_add_u32 s66, s66, s65
	s_and_b32 s12, s12, 1
	s_lshl_b32 s0, s0, 1
	s_add_u32 s0, s0, s12
	s_and_b32 s65, s13, 1
	s_lshr_b32 s13, s13, 1
	s_mul_i32 s12, s13, 0x1c00000
	s_add_u32 s12, s12, 0x4a000000
	s_lshr_b32 s13, s0, 2
	s_lshl_b32 s13, s13, 8
	s_lshl_b32 s65, s65, 7
	s_add_u32 s13, s13, s65
	s_and_b32 s65, s0, 3
	s_lshl_b32 s65, s65, 5
	s_add_u32 s13, s13, s65
	s_lshl_b32 s13, s13, 11
	s_add_u32 s12, s12, s13
	s_lshl_b32 s13, s66, 5
	s_add_u32 s12, s12, s13
	v_readlane_b32 s32, v255, 52
	v_readlane_b32 s33, v255, 53
	s_add_u32 s32, s32, s12
	s_addc_u32 s33, s33, 0
	s_movk_i32 s1, 0x800
	s_mov_b32 s0, 0x42000000
	s_branch .Lcn_dd_n0xad

; __device__ __forceinline__ void nsa_unit(const Args& a, LAS unsigned char* lds, int b, int kvh, int qb) {
;     ...
;     }
;     if (w < 4) asm volatile("s_barrier" ::: "memory");
;     __syncthreads();
.Lcn_snone_n0xb:
.Lcn_xnone_n0:
	v_and_b32_e32 v220, 0x1c0, v0
	v_lshlrev_b32_e32 v220, 6, v220
	v_and_b32_e32 v221, 63, v0
	v_lshlrev_b32_e32 v221, 2, v221
	v_add_u32_e32 v220, v220, v221
	v_add_u32_e32 v220, 0x1c000, v220
	ds_read_b32 v234, v220 offset:0
	ds_read_b32 v235, v220 offset:256
	ds_read_b32 v236, v220 offset:512
	ds_read_b32 v237, v220 offset:768
	ds_read_b32 v238, v220 offset:1024
	ds_read_b32 v239, v220 offset:1280
	ds_read_b32 v240, v220 offset:1536
	ds_read_b32 v241, v220 offset:1792
	ds_read_b32 v242, v220 offset:2048
	ds_read_b32 v243, v220 offset:2304
	ds_read_b32 v226, v220 offset:2560
	ds_read_b32 v227, v220 offset:2816
	ds_read_b32 v246, v220 offset:3072
	ds_read_b32 v247, v220 offset:3328
	ds_read_b32 v245, v220 offset:3584
	ds_read_b32 v248, v220 offset:3840
	s_waitcnt lgkmcnt(0)

; __device__ __forceinline__ void p0_weights(const Args& a, LAS unsigned char* lds) {
;     ...
;         else if ((r -= I_FD) < 16 * I_MG) { const int up = r / (8 * I_MG); r -= up * 8 * I_MG; const int e = r / I_MG; r -= e * I_MG; W = a.in[up ? I_MWU : I_MWG] + (size_t)e * D * DFE; w.K = D; w.N = DFE;
;             w.dst = a.ws + WS_MGU_T + (size_t)e * 2 * DFE * D * (MOE_FP8 ? 1 : 2); w.kind = 2 + up; w.f8 = MOE_FP8; w.scale = F8_WGU; }
;         else { r -= 16 * I_MG; const int e = r / I_MD; r -= e * I_MD; W = a.in[I_MWD] + (size_t)e * DFE * D; w.K = DFE; w.N = D; w.dst = a.ws + WS_MD_T + (size_t)e * D * DFE * (MOE_FP8 ? 1 : 2); w.f8 = MOE_FP8; w.scale = F8_WD; }
;         const int nblk = (w.N + 31) >> 5, kb = r / nblk, nb = r - kb * nblk;
;         w.k0 = 128 * kb + 16 * (lane >> 3); w.n = 32 * nb + 4 * (lane & 7); w.valid = w.n < w.N; w.src = W + (size_t)w.k0 * w.N + w.n;
; __device__ __forceinline__ void nsa_unit(const Args& a, LAS unsigned char* lds, int b, int kvh, int qb) {
;     ...
; #pragma unroll
;     for (int dt = 0; dt < 4; ++dt)
; #pragma unroll
;         for (int i = 0; i < 16; ++i) o[dt][i] = 0.f;
;     float mrun = -1e30f, lrun = 0.f;
;     f32x16 p0, p1;
; #pragma unroll
;     for (int i = 0; i < 16; ++i) { p0[i] = 0.f; p1[i] = 0.f; }
;     bf16x8 pf[2][2];
;     if (w >= 4) asm volatile("s_barrier" ::: "memory");
.LBB0_1840:
	s_cmp_lt_i32 s17, -1
	s_cbranch_scc1 .LBB0_1865
	v_mov_b32_e32 v49, v47
	s_lshl_b32 s0, s62, 1
	s_max_i32 s1, s62, 8
	v_mov_b32_e32 v60, v47
	v_mov_b32_e32 v61, v47
	v_lshl_add_u64 v[206:207], s[30:31], 0, v[48:49]
	s_sub_i32 s69, s0, s1
	v_mov_b32_e32 v46, v47
	v_mov_b32_e32 v48, v47
	v_mov_b32_e32 v50, v47
	v_mov_b32_e32 v51, v47
	v_mov_b32_e32 v52, v47
	v_mov_b32_e32 v53, v47
	v_mov_b32_e32 v54, v47
	v_mov_b32_e32 v55, v47
	v_mov_b32_e32 v56, v47
	v_mov_b32_e32 v57, v47
	v_mov_b32_e32 v58, v47
	v_mov_b32_e32 v59, v47
	v_mov_b64_e32 v[108:109], v[60:61]
	v_mov_b64_e32 v[124:125], v[60:61]
	v_mov_b64_e32 v[140:141], v[60:61]
	v_mov_b64_e32 v[156:157], v[60:61]
	v_mov_b64_e32 v[76:77], v[60:61]
	v_mov_b64_e32 v[92:93], v[60:61]
	v_add_u32_e32 v43, 1, v249
	s_add_i32 s56, s69, 11
	s_add_i32 s57, s69, 10
	s_mov_b32 s68, 2
	s_add_i32 s69, s69, 2
	s_mov_b32 s70, 0
	v_mov_b32_e32 v208, 0xf149f2ca
	v_mov_b32_e32 v209, 0
	s_movk_i32 s71, 0xc000
	v_mov_b64_e32 v[106:107], v[58:59]
	v_mov_b64_e32 v[104:105], v[56:57]
	v_mov_b64_e32 v[102:103], v[54:55]
	v_mov_b64_e32 v[100:101], v[52:53]
	v_mov_b64_e32 v[98:99], v[50:51]
	v_mov_b64_e32 v[96:97], v[48:49]
	v_mov_b64_e32 v[94:95], v[46:47]
	v_mov_b64_e32 v[122:123], v[58:59]
	v_mov_b64_e32 v[120:121], v[56:57]
	v_mov_b64_e32 v[118:119], v[54:55]
	v_mov_b64_e32 v[116:117], v[52:53]
	v_mov_b64_e32 v[114:115], v[50:51]
	v_mov_b64_e32 v[112:113], v[48:49]
	v_mov_b64_e32 v[110:111], v[46:47]
	v_mov_b64_e32 v[138:139], v[58:59]
	v_mov_b64_e32 v[136:137], v[56:57]
	v_mov_b64_e32 v[134:135], v[54:55]
	v_mov_b64_e32 v[132:133], v[52:53]
	v_mov_b64_e32 v[130:131], v[50:51]
	v_mov_b64_e32 v[128:129], v[48:49]
	v_mov_b64_e32 v[126:127], v[46:47]
	v_mov_b64_e32 v[154:155], v[58:59]
	v_mov_b64_e32 v[152:153], v[56:57]
	v_mov_b64_e32 v[150:151], v[54:55]
	v_mov_b64_e32 v[148:149], v[52:53]
	v_mov_b64_e32 v[146:147], v[50:51]
	v_mov_b64_e32 v[144:145], v[48:49]
	v_mov_b64_e32 v[142:143], v[46:47]
	v_mov_b64_e32 v[74:75], v[58:59]
	v_mov_b64_e32 v[72:73], v[56:57]
	v_mov_b64_e32 v[70:71], v[54:55]
	v_mov_b64_e32 v[68:69], v[52:53]
	v_mov_b64_e32 v[66:67], v[50:51]
	v_mov_b64_e32 v[64:65], v[48:49]
	v_mov_b64_e32 v[62:63], v[46:47]
	v_mov_b64_e32 v[90:91], v[58:59]
	v_mov_b64_e32 v[88:89], v[56:57]
	v_mov_b64_e32 v[86:87], v[54:55]
	v_mov_b64_e32 v[84:85], v[52:53]
	v_mov_b64_e32 v[82:83], v[50:51]
	v_mov_b64_e32 v[80:81], v[48:49]
	v_mov_b64_e32 v[78:79], v[46:47]
	v_and_b32_e32 v212, 0x1c0, v0
	v_lshlrev_b32_e32 v212, 6, v212
	v_and_b32_e32 v213, 63, v0
	v_lshlrev_b32_e32 v213, 2, v213
	v_add_u32_e32 v212, v212, v213
	v_add_u32_e32 v212, 0x1c000, v212
	ds_write_b32 v212, v228 offset:0
	ds_write_b32 v212, v229 offset:256
	ds_write_b32 v212, v230 offset:512
	ds_write_b32 v212, v231 offset:768
	ds_write_b32 v212, v236 offset:1024
	ds_write_b32 v212, v237 offset:1280
	ds_write_b32 v212, v238 offset:1536
	ds_write_b32 v212, v239 offset:1792
	ds_write_b32 v212, v240 offset:2048
	ds_write_b32 v212, v241 offset:2304
	ds_write_b32 v212, v242 offset:2560
	ds_write_b32 v212, v243 offset:2816
	ds_write_b32 v212, v246 offset:3072
	ds_write_b32 v212, v247 offset:3328
	ds_write_b32 v212, v245 offset:3584
	ds_write_b32 v212, v248 offset:3840
	s_waitcnt lgkmcnt(0)
	s_bitset0_b32 s101, 31
	s_bitset0_b32 s101, 30
	s_and_b32 s14, s101, 0x3fffffff
	s_cmp_ge_u32 s14, 168
	s_cbranch_scc1 .Lcn_ldum_n1sa
	s_and_b32 s14, s101, 0x3fffffff
	s_mul_i32 s15, s14, 0x2493
	s_lshr_b32 s15, s15, 16
	s_mul_i32 vcc_lo, s15, 7
	s_sub_u32 vcc_lo, s14, vcc_lo
	s_lshl_b32 vcc_lo, vcc_lo, 8
	s_lshr_b32 vcc_hi, s100, 3
	s_add_u32 vcc_lo, vcc_lo, vcc_hi
	s_and_b32 s14, s100, 7
	s_cmp_ge_u32 s15, 16
	s_cbranch_scc1 .Lcn_dn_n1sas
	s_lshr_b32 vcc_hi, vcc_lo, 4
	s_mul_i32 vcc_hi, vcc_hi, 0x2493
	s_lshr_b32 vcc_hi, vcc_hi, 16
	s_mul_i32 s0, vcc_hi, 0x70
	s_sub_u32 s0, vcc_lo, s0
	s_lshr_b32 vcc_lo, s14, 1
	s_lshl_b32 vcc_hi, vcc_hi, 2
	s_add_u32 vcc_hi, vcc_hi, vcc_lo
	s_and_b32 s14, s14, 1
	s_lshl_b32 s0, s0, 1
	s_add_u32 s0, s0, s14
	s_and_b32 vcc_lo, s15, 1
	s_lshr_b32 s15, s15, 1
	s_mul_i32 s14, s15, 0x3800000
	s_mul_i32 s15, vcc_hi, 0xe0000
	s_add_u32 s14, s14, s15
	s_lshl_b32 s15, s0, 7
	s_add_u32 s14, s14, s15
	v_readlane_b32 s32, v255, 46
	v_readlane_b32 s33, v255, 47
	s_cmp_eq_u32 vcc_lo, 0
	s_cselect_b32 s32, s98, s32
	s_cselect_b32 s33, s99, s33
	s_add_u32 s32, s32, s14
	s_addc_u32 s33, s33, 0
	s_movk_i32 s1, 0x7000
	s_branch .Lcn_dd_n1sas
.Lcn_dn_n1sas:
	s_sub_u32 s15, s15, 16
	s_lshr_b32 vcc_hi, vcc_lo, 5
	s_and_b32 s0, vcc_lo, 31
	s_lshr_b32 vcc_lo, s14, 1
	s_lshl_b32 vcc_hi, vcc_hi, 2
	s_add_u32 vcc_hi, vcc_hi, vcc_lo
	s_and_b32 s14, s14, 1
	s_lshl_b32 s0, s0, 1
	s_add_u32 s0, s0, s14
	s_mul_i32 s14, s15, 0x3800000
	s_lshl_b32 s15, vcc_hi, 18
	s_add_u32 s14, s14, s15
	s_lshl_b32 s15, s0, 7
	s_add_u32 s14, s14, s15
	v_readlane_b32 s32, v255, 48
	v_readlane_b32 s33, v255, 49
	s_add_u32 s32, s32, s14
	s_addc_u32 s33, s33, 0
	s_movk_i32 s1, 0x2000

; __device__ __forceinline__ void witem_load(const WItem& w, f32x4 (&v)[16]) {
;     if (!w.valid) return;
; #pragma unroll
;     for (int i = 0; i < 16; ++i) v[i] = *(const f32x4*)(w.src + (size_t)i * w.N);
; }
; __device__ __forceinline__ void p0_weights(const Args& a, LAS unsigned char* lds) {
;     ...
;         else if ((r -= I_FD) < 16 * I_MG) { const int up = r / (8 * I_MG); r -= up * 8 * I_MG; const int e = r / I_MG; r -= e * I_MG; W = a.in[up ? I_MWU : I_MWG] + (size_t)e * D * DFE; w.K = D; w.N = DFE;
;             w.dst = a.ws + WS_MGU_T + (size_t)e * 2 * DFE * D * (MOE_FP8 ? 1 : 2); w.kind = 2 + up; w.f8 = MOE_FP8; w.scale = F8_WGU; }
;         else { r -= 16 * I_MG; const int e = r / I_MD; r -= e * I_MD; W = a.in[I_MWD] + (size_t)e * DFE * D; w.K = DFE; w.N = D; w.dst = a.ws + WS_MD_T + (size_t)e * D * DFE * (MOE_FP8 ? 1 : 2); w.f8 = MOE_FP8; w.scale = F8_WD; }
;         const int nblk = (w.N + 31) >> 5, kb = r / nblk, nb = r - kb * nblk;
;         w.k0 = 128 * kb + 16 * (lane >> 3); w.n = 32 * nb + 4 * (lane & 7); w.valid = w.n < w.N; w.src = W + (size_t)w.k0 * w.N + w.n;
.Lcn_lgo_n1sa:
	v_and_b32_e32 v220, 63, v0
	v_and_b32_e32 v253, 7, v220
	v_lshrrev_b32_e32 v220, 3, v220
	v_lshlrev_b32_e32 v220, 2, v220
	v_lshlrev_b32_e32 v221, 4, v253
	v_lshlrev_b32_e32 v253, 2, v253
	v_mad_u32_u24 v254, v220, s1, v221
	global_load_dwordx4 v[212:215], v254, s[32:33] nt
	s_add_u32 s32, s32, s1
	s_addc_u32 s33, s33, 0
	global_load_dwordx4 v[216:219], v254, s[32:33] nt
	s_add_u32 s32, s32, s1
	s_addc_u32 s33, s33, 0
	global_load_dwordx4 v[224:227], v254, s[32:33] nt
	s_add_u32 s32, s32, s1
	s_addc_u32 s33, s33, 0
	global_load_dwordx2 v[220:221], v254, s[32:33] offset:0 nt
	global_load_dword v253, v254, s[32:33] offset:8 nt
	global_load_dword v254, v254, s[32:33] offset:12 nt
	s_and_b32 s14, s101, 0x3fffffff
	s_cmp_ge_u32 s14, 168
	s_cbranch_scc1 .Lcn_ldum_n1sb
	s_and_b32 s14, s101, 0x3fffffff
	s_mul_i32 s15, s14, 0x2493
	s_lshr_b32 s15, s15, 16
	s_mul_i32 vcc_lo, s15, 7
	s_sub_u32 vcc_lo, s14, vcc_lo
	s_lshl_b32 vcc_lo, vcc_lo, 8
	s_lshr_b32 vcc_hi, s100, 3
	s_add_u32 vcc_lo, vcc_lo, vcc_hi
	s_and_b32 s14, s100, 7
	s_cmp_ge_u32 s15, 16
	s_cbranch_scc1 .Lcn_dn_n1sbs
	s_lshr_b32 vcc_hi, vcc_lo, 4
	s_mul_i32 vcc_hi, vcc_hi, 0x2493
	s_lshr_b32 vcc_hi, vcc_hi, 16
	s_mul_i32 s0, vcc_hi, 0x70
	s_sub_u32 s0, vcc_lo, s0
	s_lshr_b32 vcc_lo, s14, 1
	s_lshl_b32 vcc_hi, vcc_hi, 2
	s_add_u32 vcc_hi, vcc_hi, vcc_lo
	s_and_b32 s14, s14, 1
	s_lshl_b32 s0, s0, 1
	s_add_u32 s0, s0, s14
	s_and_b32 vcc_lo, s15, 1
	s_lshr_b32 s15, s15, 1
	s_mul_i32 s14, s15, 0x3800000
	s_mul_i32 s15, vcc_hi, 0xe0000
	s_add_u32 s14, s14, s15
	s_lshl_b32 s15, s0, 7
	s_add_u32 s14, s14, s15
	v_readlane_b32 s32, v255, 46
	v_readlane_b32 s33, v255, 47
	s_cmp_eq_u32 vcc_lo, 0
	s_cselect_b32 s32, s98, s32
	s_cselect_b32 s33, s99, s33
	s_add_u32 s32, s32, s14
	s_addc_u32 s33, s33, 0
	s_movk_i32 s1, 0x7000
	s_branch .Lcn_dd_n1sbs

; __device__ __forceinline__ void witem_load(const WItem& w, f32x4 (&v)[16]) {
;     if (!w.valid) return;
; #pragma unroll
;     for (int i = 0; i < 16; ++i) v[i] = *(const f32x4*)(w.src + (size_t)i * w.N);
; }
; __device__ __forceinline__ void nsa_unit(const Args& a, LAS unsigned char* lds, int b, int kvh, int qb) {
;     ...
;     for (int it = 0; it <= nTot; ++it) {
;         if (it + 1 < nTot) asm volatile("s_waitcnt vmcnt(4) lgkmcnt(0)\n\ts_barrier" ::: "memory"); else asm volatile("s_waitcnt vmcnt(0) lgkmcnt(0)\n\ts_barrier" ::: "memory");
.Lcn_lgo_n1sb:
	v_and_b32_e32 v246, 63, v0
	v_and_b32_e32 v245, 7, v246
	v_lshrrev_b32_e32 v246, 3, v246
	v_lshlrev_b32_e32 v246, 2, v246
	v_lshlrev_b32_e32 v247, 4, v245
	v_lshlrev_b32_e32 v245, 2, v245
	v_mad_u32_u24 v248, v246, s1, v247
	global_load_dwordx4 v[228:231], v248, s[32:33] nt
	s_add_u32 s32, s32, s1
	s_addc_u32 s33, s33, 0
	global_load_dwordx4 v[236:239], v248, s[32:33] nt
	s_add_u32 s32, s32, s1
	s_addc_u32 s33, s33, 0
	global_load_dwordx4 v[240:243], v248, s[32:33] nt
	s_add_u32 s32, s32, s1
	s_addc_u32 s33, s33, 0
	global_load_dwordx2 v[246:247], v248, s[32:33] offset:0 nt
	global_load_dword v245, v248, s[32:33] offset:8 nt
	global_load_dword v248, v248, s[32:33] offset:12 nt
	s_branch .LBB0_1843
.LBB0_1842:
	s_bitcmp1_b32 s101, 31
	s_cbranch_scc1 .Lcn_lB_n1
	s_bitcmp1_b32 s101, 30
	s_cbranch_scc1 .Lcn_wf_n1A
	s_add_i32 s14, s70, 2
	s_cmp_gt_i32 s14, s17
	s_cbranch_scc1 .Lcn_w0_n1A0
	s_waitcnt vmcnt(10)
	s_branch .Lcn_wd_n1A
.Lcn_w0_n1A0:
	s_cmp_gt_i32 s70, s17
	s_cbranch_scc1 .Lcn_w1_n1A0
	s_waitcnt vmcnt(6)
	s_branch .Lcn_wd_n1A

; __device__ __forceinline__ void nsa_unit(const Args& a, LAS unsigned char* lds, int b, int kvh, int qb) {
;     ...
;     for (int it = 0; it <= nTot; ++it) {
;         if (it + 1 < nTot) asm volatile("s_waitcnt vmcnt(4) lgkmcnt(0)\n\ts_barrier" ::: "memory"); else asm volatile("s_waitcnt vmcnt(0) lgkmcnt(0)\n\ts_barrier" ::: "memory");
.Lcn_wf_n1A:
	s_add_i32 s14, s70, 2
	s_cmp_gt_i32 s14, s17
	s_cbranch_scc1 .Lcn_w0_n1A1
	s_waitcnt vmcnt(14)
	s_branch .Lcn_wd_n1A
.Lcn_w0_n1A1:
	s_cmp_gt_i32 s70, s17
	s_cbranch_scc1 .Lcn_w1_n1A1
	s_waitcnt vmcnt(10)
	s_branch .Lcn_wd_n1A

; __device__ __forceinline__ unsigned pk4_fp8(float a, float b, float c, float d) { int p = __builtin_amdgcn_cvt_pk_fp8_f32(a, b, 0, false); p = __builtin_amdgcn_cvt_pk_fp8_f32(c, d, p, true); return (unsigned)p; }
; __device__ __forceinline__ void witem_store(const WItem& w, const f32x4 (&v)[16]) {
;     if (!w.valid) return;
;     if (w.f8) {
; #pragma unroll
;         for (int j = 0; j < 4; ++j) { u32x4 o; const float sc = w.scale;
;             o.x = pk4_fp8(v[0][j] * sc, v[1][j] * sc, v[2][j] * sc, v[3][j] * sc); o.y = pk4_fp8(v[4][j] * sc, v[5][j] * sc, v[6][j] * sc, v[7][j] * sc);
;             o.z = pk4_fp8(v[8][j] * sc, v[9][j] * sc, v[10][j] * sc, v[11][j] * sc); o.w = pk4_fp8(v[12][j] * sc, v[13][j] * sc, v[14][j] * sc, v[15][j] * sc);
;             *(u32x4*)(w.dst + (size_t)witem_row(w.kind, w.n + j) * w.K + w.k0) = o; }
; __device__ __forceinline__ void p0_weights(const Args& a, LAS unsigned char* lds) {
;     ...
;         else if ((r -= I_FD) < 16 * I_MG) { const int up = r / (8 * I_MG); r -= up * 8 * I_MG; const int e = r / I_MG; r -= e * I_MG; W = a.in[up ? I_MWU : I_MWG] + (size_t)e * D * DFE; w.K = D; w.N = DFE;
;             w.dst = a.ws + WS_MGU_T + (size_t)e * 2 * DFE * D * (MOE_FP8 ? 1 : 2); w.kind = 2 + up; w.f8 = MOE_FP8; w.scale = F8_WGU; }
;         else { r -= 16 * I_MG; const int e = r / I_MD; r -= e * I_MD; W = a.in[I_MWD] + (size_t)e * DFE * D; w.K = DFE; w.N = D; w.dst = a.ws + WS_MD_T + (size_t)e * D * DFE * (MOE_FP8 ? 1 : 2); w.f8 = MOE_FP8; w.scale = F8_WD; }
;         const int nblk = (w.N + 31) >> 5, kb = r / nblk, nb = r - kb * nblk;
;         w.k0 = 128 * kb + 16 * (lane >> 3); w.n = 32 * nb + 4 * (lane & 7); w.valid = w.n < w.N; w.src = W + (size_t)w.k0 * w.N + w.n;
.Lcn_wd_n1A:
	s_bitset0_b32 s101, 30
	s_bitcmp1_b32 s25, 31
	s_cbranch_scc0 .Lcn_snone_n1Al
	s_and_b32 s14, s25, 0x3fffffff
	s_mul_i32 s15, s14, 0x2493
	s_lshr_b32 s15, s15, 16
	s_mul_i32 vcc_lo, s15, 7
	s_sub_u32 vcc_lo, s14, vcc_lo
	s_lshl_b32 vcc_lo, vcc_lo, 8
	s_lshr_b32 vcc_hi, s100, 3
	s_add_u32 vcc_lo, vcc_lo, vcc_hi
	s_and_b32 s14, s100, 7
	s_cmp_ge_u32 s15, 16
	s_cbranch_scc1 .Lcn_dn_n1Ald
	s_lshr_b32 vcc_hi, vcc_lo, 4
	s_mul_i32 vcc_hi, vcc_hi, 0x2493
	s_lshr_b32 vcc_hi, vcc_hi, 16
	s_mul_i32 s0, vcc_hi, 0x70
	s_sub_u32 s0, vcc_lo, s0
	s_lshr_b32 vcc_lo, s14, 1
	s_lshl_b32 vcc_hi, vcc_hi, 2
	s_add_u32 vcc_hi, vcc_hi, vcc_lo
	s_and_b32 s14, s14, 1
	s_lshl_b32 s0, s0, 1
	s_add_u32 s0, s0, s14
	s_and_b32 vcc_lo, s15, 1
	s_lshr_b32 s15, s15, 1
	s_mul_i32 s14, s15, 0x1c00000
	s_add_u32 s14, s14, 0x4a000000
	s_lshr_b32 s15, s0, 2
	s_lshl_b32 s15, s15, 8
	s_lshl_b32 vcc_lo, vcc_lo, 7
	s_add_u32 s15, s15, vcc_lo
	s_and_b32 vcc_lo, s0, 3
	s_lshl_b32 vcc_lo, vcc_lo, 5
	s_add_u32 s15, s15, vcc_lo
	s_lshl_b32 s15, s15, 11
	s_add_u32 s14, s14, s15
	s_lshl_b32 s15, vcc_hi, 5
	s_add_u32 s14, s14, s15
	v_readlane_b32 s32, v255, 52
	v_readlane_b32 s33, v255, 53
	s_add_u32 s32, s32, s14
	s_addc_u32 s33, s33, 0
	s_movk_i32 s1, 0x800
	s_mov_b32 s0, 0x42000000
	s_branch .Lcn_dd_n1Ald
.Lcn_dn_n1Ald:
	s_sub_u32 s15, s15, 16
	s_lshr_b32 vcc_hi, vcc_lo, 5
	s_and_b32 s0, vcc_lo, 31
	s_lshr_b32 vcc_lo, s14, 1
	s_lshl_b32 vcc_hi, vcc_hi, 2
	s_add_u32 vcc_hi, vcc_hi, vcc_lo
	s_and_b32 s14, s14, 1
	s_lshl_b32 s0, s0, 1
	s_add_u32 s0, s0, s14
	s_mul_i32 s14, s15, 0xe00000
	s_add_u32 s14, s14, 0x66000000
	s_mul_i32 s15, s0, 0x38000
	s_add_u32 s14, s14, s15
	s_lshl_b32 s15, vcc_hi, 5
	s_add_u32 s14, s14, s15
	v_readlane_b32 s32, v255, 52
	v_readlane_b32 s33, v255, 53
	s_add_u32 s32, s32, s14
	s_addc_u32 s33, s33, 0
	s_movk_i32 s1, 0x1c00
	s_mov_b32 s0, 0x43000000
.Lcn_dd_n1Ald:
	s_mov_b32 s25, 0
	s_bitset1_b32 s101, 30
	v_mul_f32_e32 v212, s0, v212
	v_mul_f32_e32 v213, s0, v213
	v_mul_f32_e32 v214, s0, v214
	v_mul_f32_e32 v215, s0, v215
	v_mul_f32_e32 v216, s0, v216
	v_mul_f32_e32 v217, s0, v217
	v_mul_f32_e32 v218, s0, v218
	v_mul_f32_e32 v219, s0, v219
	v_mul_f32_e32 v224, s0, v224
	v_mul_f32_e32 v225, s0, v225
	v_mul_f32_e32 v226, s0, v226
	v_mul_f32_e32 v227, s0, v227
	v_mul_f32_e32 v220, s0, v220
	v_mul_f32_e32 v221, s0, v221
	v_mul_f32_e32 v253, s0, v253
	v_mul_f32_e32 v254, s0, v254
	v_cvt_pk_fp8_f32 v212, v212, v216
	v_cvt_pk_fp8_f32 v213, v213, v217
	v_cvt_pk_fp8_f32 v214, v214, v218
	v_cvt_pk_fp8_f32 v215, v215, v219
	v_cvt_pk_fp8_f32 v212, v224, v220 op_sel:[0,0,1]
	v_cvt_pk_fp8_f32 v213, v225, v221 op_sel:[0,0,1]
	v_cvt_pk_fp8_f32 v214, v226, v253 op_sel:[0,0,1]
	v_cvt_pk_fp8_f32 v215, v227, v254 op_sel:[0,0,1]
	v_and_b32_e32 v216, 63, v0
	v_and_b32_e32 v218, 7, v216
	v_lshrrev_b32_e32 v216, 3, v216
	v_lshlrev_b32_e32 v216, 2, v216
	v_lshlrev_b32_e32 v217, 4, v218
	v_lshlrev_b32_e32 v218, 2, v218
	v_mad_u32_u24 v217, v218, s1, v216
	global_store_dword v217, v212, s[32:33] nt
	v_add_u32_e32 v216, s1, v217
	global_store_dword v216, v213, s[32:33] nt
	v_add_u32_e32 v218, s1, v216
	global_store_dword v218, v214, s[32:33] nt
	v_add_u32_e32 v219, s1, v218
	global_store_dword v219, v215, s[32:33] nt
.Lcn_snone_n1Al:
	s_mov_b32 s25, 0
	s_add_i32 s14, s70, 1
	s_cmp_gt_i32 s14, s17
	s_cbranch_scc1 .Lcn_lskip_n1Al
	s_and_b32 s14, s101, 0x3fffffff
	s_cmp_ge_u32 s14, 168
	s_cbranch_scc1 .Lcn_ldum_n1Al
	s_and_b32 s14, s101, 0x3fffffff
	s_mul_i32 s15, s14, 0x2493
	s_lshr_b32 s15, s15, 16
	s_mul_i32 vcc_lo, s15, 7
	s_sub_u32 vcc_lo, s14, vcc_lo
	s_lshl_b32 vcc_lo, vcc_lo, 8
	s_lshr_b32 vcc_hi, s100, 3
	s_add_u32 vcc_lo, vcc_lo, vcc_hi
	s_and_b32 s14, s100, 7
	s_cmp_ge_u32 s15, 16
	s_cbranch_scc1 .Lcn_dn_n1Als
	s_lshr_b32 vcc_hi, vcc_lo, 4
	s_mul_i32 vcc_hi, vcc_hi, 0x2493
	s_lshr_b32 vcc_hi, vcc_hi, 16
	s_mul_i32 s0, vcc_hi, 0x70
	s_sub_u32 s0, vcc_lo, s0
	s_lshr_b32 vcc_lo, s14, 1
	s_lshl_b32 vcc_hi, vcc_hi, 2
	s_add_u32 vcc_hi, vcc_hi, vcc_lo
	s_and_b32 s14, s14, 1
	s_lshl_b32 s0, s0, 1
	s_add_u32 s0, s0, s14
	s_and_b32 vcc_lo, s15, 1
	s_lshr_b32 s15, s15, 1
	s_mul_i32 s14, s15, 0x3800000
	s_mul_i32 s15, vcc_hi, 0xe0000
	s_add_u32 s14, s14, s15
	s_lshl_b32 s15, s0, 7
	s_add_u32 s14, s14, s15
	v_readlane_b32 s32, v255, 46
	v_readlane_b32 s33, v255, 47
	s_cmp_eq_u32 vcc_lo, 0
	s_cselect_b32 s32, s98, s32
	s_cselect_b32 s33, s99, s33
	s_add_u32 s32, s32, s14
	s_addc_u32 s33, s33, 0
	s_movk_i32 s1, 0x7000
	s_branch .Lcn_dd_n1Als

; __device__ __forceinline__ void witem_load(const WItem& w, f32x4 (&v)[16]) {
;     if (!w.valid) return;
; #pragma unroll
;     for (int i = 0; i < 16; ++i) v[i] = *(const f32x4*)(w.src + (size_t)i * w.N);
; }
.Lcn_lgo_n1Al:
	v_and_b32_e32 v220, 63, v0
	v_and_b32_e32 v253, 7, v220
	v_lshrrev_b32_e32 v220, 3, v220
	v_lshlrev_b32_e32 v220, 2, v220
	v_lshlrev_b32_e32 v221, 4, v253
	v_lshlrev_b32_e32 v253, 2, v253
	v_mad_u32_u24 v254, v220, s1, v221
	global_load_dwordx4 v[212:215], v254, s[32:33] nt
	s_add_u32 s32, s32, s1
	s_addc_u32 s33, s33, 0
	global_load_dwordx4 v[216:219], v254, s[32:33] nt
	s_add_u32 s32, s32, s1
	s_addc_u32 s33, s33, 0
	global_load_dwordx4 v[224:227], v254, s[32:33] nt
	s_add_u32 s32, s32, s1
	s_addc_u32 s33, s33, 0
	global_load_dwordx2 v[220:221], v254, s[32:33] offset:0 nt
	global_load_dword v253, v254, s[32:33] offset:8 nt
	global_load_dword v254, v254, s[32:33] offset:12 nt

; __device__ __forceinline__ void nsa_unit(const Args& a, LAS unsigned char* lds, int b, int kvh, int qb) {
;     ...
;     for (int it = 0; it <= nTot; ++it) {
;         if (it + 1 < nTot) asm volatile("s_waitcnt vmcnt(4) lgkmcnt(0)\n\ts_barrier" ::: "memory"); else asm volatile("s_waitcnt vmcnt(0) lgkmcnt(0)\n\ts_barrier" ::: "memory");
.Lcn_lB_n1:
	s_bitcmp1_b32 s101, 30
	s_cbranch_scc1 .Lcn_wf_n1B
	s_add_i32 s14, s70, 2
	s_cmp_gt_i32 s14, s17
	s_cbranch_scc1 .Lcn_w0_n1B0
	s_waitcnt vmcnt(10)
	s_branch .Lcn_wd_n1B

; __device__ __forceinline__ void p0_weights(const Args& a, LAS unsigned char* lds) {
;     ...
;         else if ((r -= I_FD) < 16 * I_MG) { const int up = r / (8 * I_MG); r -= up * 8 * I_MG; const int e = r / I_MG; r -= e * I_MG; W = a.in[up ? I_MWU : I_MWG] + (size_t)e * D * DFE; w.K = D; w.N = DFE;
;             w.dst = a.ws + WS_MGU_T + (size_t)e * 2 * DFE * D * (MOE_FP8 ? 1 : 2); w.kind = 2 + up; w.f8 = MOE_FP8; w.scale = F8_WGU; }
;         else { r -= 16 * I_MG; const int e = r / I_MD; r -= e * I_MD; W = a.in[I_MWD] + (size_t)e * DFE * D; w.K = DFE; w.N = D; w.dst = a.ws + WS_MD_T + (size_t)e * D * DFE * (MOE_FP8 ? 1 : 2); w.f8 = MOE_FP8; w.scale = F8_WD; }
;         const int nblk = (w.N + 31) >> 5, kb = r / nblk, nb = r - kb * nblk;
;         w.k0 = 128 * kb + 16 * (lane >> 3); w.n = 32 * nb + 4 * (lane & 7); w.valid = w.n < w.N; w.src = W + (size_t)w.k0 * w.N + w.n;
.Lcn_wd_n1B:
	s_bitset0_b32 s101, 30
	s_bitcmp1_b32 s67, 31
	s_cbranch_scc0 .Lcn_snone_n1Bl
	s_and_b32 s14, s67, 0x3fffffff
	s_mul_i32 s15, s14, 0x2493
	s_lshr_b32 s15, s15, 16
	s_mul_i32 vcc_lo, s15, 7
	s_sub_u32 vcc_lo, s14, vcc_lo
	s_lshl_b32 vcc_lo, vcc_lo, 8
	s_lshr_b32 vcc_hi, s100, 3
	s_add_u32 vcc_lo, vcc_lo, vcc_hi
	s_and_b32 s14, s100, 7
	s_cmp_ge_u32 s15, 16
	s_cbranch_scc1 .Lcn_dn_n1Bld
	s_lshr_b32 vcc_hi, vcc_lo, 4
	s_mul_i32 vcc_hi, vcc_hi, 0x2493
	s_lshr_b32 vcc_hi, vcc_hi, 16
	s_mul_i32 s0, vcc_hi, 0x70
	s_sub_u32 s0, vcc_lo, s0
	s_lshr_b32 vcc_lo, s14, 1
	s_lshl_b32 vcc_hi, vcc_hi, 2
	s_add_u32 vcc_hi, vcc_hi, vcc_lo
	s_and_b32 s14, s14, 1
	s_lshl_b32 s0, s0, 1
	s_add_u32 s0, s0, s14
	s_and_b32 vcc_lo, s15, 1
	s_lshr_b32 s15, s15, 1
	s_mul_i32 s14, s15, 0x1c00000
	s_add_u32 s14, s14, 0x4a000000
	s_lshr_b32 s15, s0, 2
	s_lshl_b32 s15, s15, 8
	s_lshl_b32 vcc_lo, vcc_lo, 7
	s_add_u32 s15, s15, vcc_lo
	s_and_b32 vcc_lo, s0, 3
	s_lshl_b32 vcc_lo, vcc_lo, 5
	s_add_u32 s15, s15, vcc_lo
	s_lshl_b32 s15, s15, 11
	s_add_u32 s14, s14, s15
	s_lshl_b32 s15, vcc_hi, 5
	s_add_u32 s14, s14, s15
	v_readlane_b32 s32, v255, 52
	v_readlane_b32 s33, v255, 53
	s_add_u32 s32, s32, s14
	s_addc_u32 s33, s33, 0
	s_movk_i32 s1, 0x800
	s_mov_b32 s0, 0x42000000
	s_branch .Lcn_dd_n1Bld

; __device__ __forceinline__ unsigned pk4_fp8(float a, float b, float c, float d) { int p = __builtin_amdgcn_cvt_pk_fp8_f32(a, b, 0, false); p = __builtin_amdgcn_cvt_pk_fp8_f32(c, d, p, true); return (unsigned)p; }
; __device__ __forceinline__ void witem_store(const WItem& w, const f32x4 (&v)[16]) {
;     if (!w.valid) return;
;     if (w.f8) {
; #pragma unroll
;         for (int j = 0; j < 4; ++j) { u32x4 o; const float sc = w.scale;
;             o.x = pk4_fp8(v[0][j] * sc, v[1][j] * sc, v[2][j] * sc, v[3][j] * sc); o.y = pk4_fp8(v[4][j] * sc, v[5][j] * sc, v[6][j] * sc, v[7][j] * sc);
;             o.z = pk4_fp8(v[8][j] * sc, v[9][j] * sc, v[10][j] * sc, v[11][j] * sc); o.w = pk4_fp8(v[12][j] * sc, v[13][j] * sc, v[14][j] * sc, v[15][j] * sc);
;             *(u32x4*)(w.dst + (size_t)witem_row(w.kind, w.n + j) * w.K + w.k0) = o; }
; __device__ __forceinline__ void p0_weights(const Args& a, LAS unsigned char* lds) {
;     ...
;         else if ((r -= I_FD) < 16 * I_MG) { const int up = r / (8 * I_MG); r -= up * 8 * I_MG; const int e = r / I_MG; r -= e * I_MG; W = a.in[up ? I_MWU : I_MWG] + (size_t)e * D * DFE; w.K = D; w.N = DFE;
;             w.dst = a.ws + WS_MGU_T + (size_t)e * 2 * DFE * D * (MOE_FP8 ? 1 : 2); w.kind = 2 + up; w.f8 = MOE_FP8; w.scale = F8_WGU; }
;         else { r -= 16 * I_MG; const int e = r / I_MD; r -= e * I_MD; W = a.in[I_MWD] + (size_t)e * DFE * D; w.K = DFE; w.N = D; w.dst = a.ws + WS_MD_T + (size_t)e * D * DFE * (MOE_FP8 ? 1 : 2); w.f8 = MOE_FP8; w.scale = F8_WD; }
;         const int nblk = (w.N + 31) >> 5, kb = r / nblk, nb = r - kb * nblk;
;         w.k0 = 128 * kb + 16 * (lane >> 3); w.n = 32 * nb + 4 * (lane & 7); w.valid = w.n < w.N; w.src = W + (size_t)w.k0 * w.N + w.n;
.Lcn_dd_n1Bld:
	s_mov_b32 s67, 0
	s_bitset1_b32 s101, 30
	v_mul_f32_e32 v228, s0, v228
	v_mul_f32_e32 v229, s0, v229
	v_mul_f32_e32 v230, s0, v230
	v_mul_f32_e32 v231, s0, v231
	v_mul_f32_e32 v236, s0, v236
	v_mul_f32_e32 v237, s0, v237
	v_mul_f32_e32 v238, s0, v238
	v_mul_f32_e32 v239, s0, v239
	v_mul_f32_e32 v240, s0, v240
	v_mul_f32_e32 v241, s0, v241
	v_mul_f32_e32 v242, s0, v242
	v_mul_f32_e32 v243, s0, v243
	v_mul_f32_e32 v246, s0, v246
	v_mul_f32_e32 v247, s0, v247
	v_mul_f32_e32 v245, s0, v245
	v_mul_f32_e32 v248, s0, v248
	v_cvt_pk_fp8_f32 v228, v228, v236
	v_cvt_pk_fp8_f32 v229, v229, v237
	v_cvt_pk_fp8_f32 v230, v230, v238
	v_cvt_pk_fp8_f32 v231, v231, v239
	v_cvt_pk_fp8_f32 v228, v240, v246 op_sel:[0,0,1]
	v_cvt_pk_fp8_f32 v229, v241, v247 op_sel:[0,0,1]
	v_cvt_pk_fp8_f32 v230, v242, v245 op_sel:[0,0,1]
	v_cvt_pk_fp8_f32 v231, v243, v248 op_sel:[0,0,1]
	v_and_b32_e32 v236, 63, v0
	v_and_b32_e32 v238, 7, v236
	v_lshrrev_b32_e32 v236, 3, v236
	v_lshlrev_b32_e32 v236, 2, v236
	v_lshlrev_b32_e32 v237, 4, v238
	v_lshlrev_b32_e32 v238, 2, v238
	v_mad_u32_u24 v237, v238, s1, v236
	global_store_dword v237, v228, s[32:33] nt
	v_add_u32_e32 v236, s1, v237
	global_store_dword v236, v229, s[32:33] nt
	v_add_u32_e32 v238, s1, v236
	global_store_dword v238, v230, s[32:33] nt
	v_add_u32_e32 v239, s1, v238
	global_store_dword v239, v231, s[32:33] nt
.Lcn_snone_n1Bl:
	s_mov_b32 s67, 0
	s_add_i32 s14, s70, 1
	s_cmp_gt_i32 s14, s17
	s_cbranch_scc1 .Lcn_lskip_n1Bl
	s_and_b32 s14, s101, 0x3fffffff
	s_cmp_ge_u32 s14, 168
	s_cbranch_scc1 .Lcn_ldum_n1Bl
	s_and_b32 s14, s101, 0x3fffffff
	s_mul_i32 s15, s14, 0x2493
	s_lshr_b32 s15, s15, 16
	s_mul_i32 vcc_lo, s15, 7
	s_sub_u32 vcc_lo, s14, vcc_lo
	s_lshl_b32 vcc_lo, vcc_lo, 8
	s_lshr_b32 vcc_hi, s100, 3
	s_add_u32 vcc_lo, vcc_lo, vcc_hi
	s_and_b32 s14, s100, 7
	s_cmp_ge_u32 s15, 16
	s_cbranch_scc1 .Lcn_dn_n1Bls
	s_lshr_b32 vcc_hi, vcc_lo, 4
	s_mul_i32 vcc_hi, vcc_hi, 0x2493
	s_lshr_b32 vcc_hi, vcc_hi, 16
	s_mul_i32 s0, vcc_hi, 0x70
	s_sub_u32 s0, vcc_lo, s0
	s_lshr_b32 vcc_lo, s14, 1
	s_lshl_b32 vcc_hi, vcc_hi, 2
	s_add_u32 vcc_hi, vcc_hi, vcc_lo
	s_and_b32 s14, s14, 1
	s_lshl_b32 s0, s0, 1
	s_add_u32 s0, s0, s14
	s_and_b32 vcc_lo, s15, 1
	s_lshr_b32 s15, s15, 1
	s_mul_i32 s14, s15, 0x3800000
	s_mul_i32 s15, vcc_hi, 0xe0000
	s_add_u32 s14, s14, s15
	s_lshl_b32 s15, s0, 7
	s_add_u32 s14, s14, s15
	v_readlane_b32 s32, v255, 46
	v_readlane_b32 s33, v255, 47
	s_cmp_eq_u32 vcc_lo, 0
	s_cselect_b32 s32, s98, s32
	s_cselect_b32 s33, s99, s33
	s_add_u32 s32, s32, s14
	s_addc_u32 s33, s33, 0
	s_movk_i32 s1, 0x7000
	s_branch .Lcn_dd_n1Bls

; __device__ __forceinline__ void witem_load(const WItem& w, f32x4 (&v)[16]) {
;     if (!w.valid) return;
; #pragma unroll
;     for (int i = 0; i < 16; ++i) v[i] = *(const f32x4*)(w.src + (size_t)i * w.N);
; }
.Lcn_lgo_n1Bl:
	v_and_b32_e32 v246, 63, v0
	v_and_b32_e32 v245, 7, v246
	v_lshrrev_b32_e32 v246, 3, v246
	v_lshlrev_b32_e32 v246, 2, v246
	v_lshlrev_b32_e32 v247, 4, v245
	v_lshlrev_b32_e32 v245, 2, v245
	v_mad_u32_u24 v248, v246, s1, v247
	global_load_dwordx4 v[228:231], v248, s[32:33] nt
	s_add_u32 s32, s32, s1
	s_addc_u32 s33, s33, 0
	global_load_dwordx4 v[236:239], v248, s[32:33] nt
	s_add_u32 s32, s32, s1
	s_addc_u32 s33, s33, 0
	global_load_dwordx4 v[240:243], v248, s[32:33] nt
	s_add_u32 s32, s32, s1
	s_addc_u32 s33, s33, 0
	global_load_dwordx2 v[246:247], v248, s[32:33] offset:0 nt
	global_load_dword v245, v248, s[32:33] offset:8 nt
	global_load_dword v248, v248, s[32:33] offset:12 nt

; __device__ __forceinline__ void nsa_unit(const Args& a, LAS unsigned char* lds, int b, int kvh, int qb) {
;     ...
;     for (int it = 0; it <= nTot; ++it) {
;         if (it + 1 < nTot) asm volatile("s_waitcnt vmcnt(4) lgkmcnt(0)\n\ts_barrier" ::: "memory"); else asm volatile("s_waitcnt vmcnt(0) lgkmcnt(0)\n\ts_barrier" ::: "memory");
.LBB0_1843:
	s_cmp_ge_i32 s70, s17
	s_mov_b64 s[0:1], -1
	s_cbranch_scc0 .LBB0_1846
	s_waitcnt vmcnt(12) lgkmcnt(0)
	s_barrier
	s_cbranch_execz .LBB0_1847

; __device__ __forceinline__ void nsa_unit(const Args& a, LAS unsigned char* lds, int b, int kvh, int qb) {
;     ...
;         asm volatile("s_waitcnt lgkmcnt(0)\n\ts_barrier" ::: "memory");
.LBB0_1847:
	s_waitcnt vmcnt(16) lgkmcnt(0)
	s_barrier
	s_cmp_lg_u32 s70, 0
	s_cselect_b64 s[0:1], -1, 0
	s_cmp_eq_u32 s70, 0
	s_cbranch_scc1 .LBB0_1858

; __device__ __forceinline__ void p0_weights(const Args& a, LAS unsigned char* lds) {
;     ...
;         else if ((r -= I_FD) < 16 * I_MG) { const int up = r / (8 * I_MG); r -= up * 8 * I_MG; const int e = r / I_MG; r -= e * I_MG; W = a.in[up ? I_MWU : I_MWG] + (size_t)e * D * DFE; w.K = D; w.N = DFE;
;             w.dst = a.ws + WS_MGU_T + (size_t)e * 2 * DFE * D * (MOE_FP8 ? 1 : 2); w.kind = 2 + up; w.f8 = MOE_FP8; w.scale = F8_WGU; }
;         else { r -= 16 * I_MG; const int e = r / I_MD; r -= e * I_MD; W = a.in[I_MWD] + (size_t)e * DFE * D; w.K = DFE; w.N = D; w.dst = a.ws + WS_MD_T + (size_t)e * D * DFE * (MOE_FP8 ? 1 : 2); w.f8 = MOE_FP8; w.scale = F8_WD; }
;         const int nblk = (w.N + 31) >> 5, kb = r / nblk, nb = r - kb * nblk;
;         w.k0 = 128 * kb + 16 * (lane >> 3); w.n = 32 * nb + 4 * (lane & 7); w.valid = w.n < w.N; w.src = W + (size_t)w.k0 * w.N + w.n;
.Lcn_exit_n1:
	s_or_b32 s14, s25, s67
	s_bitcmp1_b32 s14, 31
	s_cbranch_scc0 .Lcn_xnone_n1
	s_waitcnt vmcnt(0)
	s_bitset0_b32 s101, 30
	s_bitcmp1_b32 s25, 31
	s_cbranch_scc0 .Lcn_snone_n1xa
	s_and_b32 s14, s25, 0x3fffffff
	s_mul_i32 s15, s14, 0x2493
	s_lshr_b32 s15, s15, 16
	s_mul_i32 vcc_lo, s15, 7
	s_sub_u32 vcc_lo, s14, vcc_lo
	s_lshl_b32 vcc_lo, vcc_lo, 8
	s_lshr_b32 vcc_hi, s100, 3
	s_add_u32 vcc_lo, vcc_lo, vcc_hi
	s_and_b32 s14, s100, 7
	s_cmp_ge_u32 s15, 16
	s_cbranch_scc1 .Lcn_dn_n1xad
	s_lshr_b32 vcc_hi, vcc_lo, 4
	s_mul_i32 vcc_hi, vcc_hi, 0x2493
	s_lshr_b32 vcc_hi, vcc_hi, 16
	s_mul_i32 s0, vcc_hi, 0x70
	s_sub_u32 s0, vcc_lo, s0
	s_lshr_b32 vcc_lo, s14, 1
	s_lshl_b32 vcc_hi, vcc_hi, 2
	s_add_u32 vcc_hi, vcc_hi, vcc_lo
	s_and_b32 s14, s14, 1
	s_lshl_b32 s0, s0, 1
	s_add_u32 s0, s0, s14
	s_and_b32 vcc_lo, s15, 1
	s_lshr_b32 s15, s15, 1
	s_mul_i32 s14, s15, 0x1c00000
	s_add_u32 s14, s14, 0x4a000000
	s_lshr_b32 s15, s0, 2
	s_lshl_b32 s15, s15, 8
	s_lshl_b32 vcc_lo, vcc_lo, 7
	s_add_u32 s15, s15, vcc_lo
	s_and_b32 vcc_lo, s0, 3
	s_lshl_b32 vcc_lo, vcc_lo, 5
	s_add_u32 s15, s15, vcc_lo
	s_lshl_b32 s15, s15, 11
	s_add_u32 s14, s14, s15
	s_lshl_b32 s15, vcc_hi, 5
	s_add_u32 s14, s14, s15
	v_readlane_b32 s32, v255, 52
	v_readlane_b32 s33, v255, 53
	s_add_u32 s32, s32, s14
	s_addc_u32 s33, s33, 0
	s_movk_i32 s1, 0x800
	s_mov_b32 s0, 0x42000000
	s_branch .Lcn_dd_n1xad

; __device__ __forceinline__ void nsa_unit(const Args& a, LAS unsigned char* lds, int b, int kvh, int qb) {
;     ...
;     }
;     if (w < 4) asm volatile("s_barrier" ::: "memory");
;     __syncthreads();
.Lcn_snone_n1xb:
.Lcn_xnone_n1:
	v_and_b32_e32 v224, 0x1c0, v0
	v_lshlrev_b32_e32 v224, 6, v224
	v_and_b32_e32 v225, 63, v0
	v_lshlrev_b32_e32 v225, 2, v225
	v_add_u32_e32 v224, v224, v225
	v_add_u32_e32 v224, 0x1c000, v224
	ds_read_b32 v228, v224 offset:0
	ds_read_b32 v229, v224 offset:256
	ds_read_b32 v230, v224 offset:512
	ds_read_b32 v231, v224 offset:768
	ds_read_b32 v236, v224 offset:1024
	ds_read_b32 v237, v224 offset:1280
	ds_read_b32 v238, v224 offset:1536
	ds_read_b32 v239, v224 offset:1792
	ds_read_b32 v240, v224 offset:2048
	ds_read_b32 v241, v224 offset:2304
	ds_read_b32 v242, v224 offset:2560
	ds_read_b32 v243, v224 offset:2816
	ds_read_b32 v246, v224 offset:3072
	ds_read_b32 v247, v224 offset:3328
	ds_read_b32 v245, v224 offset:3584
	ds_read_b32 v248, v224 offset:3840
	s_waitcnt lgkmcnt(0)

; __device__ __forceinline__ void p0_weights(const Args& a, LAS unsigned char* lds) {
;     ...
;         else if ((r -= I_FD) < 16 * I_MG) { const int up = r / (8 * I_MG); r -= up * 8 * I_MG; const int e = r / I_MG; r -= e * I_MG; W = a.in[up ? I_MWU : I_MWG] + (size_t)e * D * DFE; w.K = D; w.N = DFE;
;             w.dst = a.ws + WS_MGU_T + (size_t)e * 2 * DFE * D * (MOE_FP8 ? 1 : 2); w.kind = 2 + up; w.f8 = MOE_FP8; w.scale = F8_WGU; }
;         else { r -= 16 * I_MG; const int e = r / I_MD; r -= e * I_MD; W = a.in[I_MWD] + (size_t)e * DFE * D; w.K = DFE; w.N = D; w.dst = a.ws + WS_MD_T + (size_t)e * D * DFE * (MOE_FP8 ? 1 : 2); w.f8 = MOE_FP8; w.scale = F8_WD; }
;         const int nblk = (w.N + 31) >> 5, kb = r / nblk, nb = r - kb * nblk;
;         w.k0 = 128 * kb + 16 * (lane >> 3); w.n = 32 * nb + 4 * (lane & 7); w.valid = w.n < w.N; w.src = W + (size_t)w.k0 * w.N + w.n;
;     ...
;     { f32x4 v[16], vn[16];
;       WItem cur = decode(gw); witem_load(cur, v);
; #pragma unroll 1
;       for (int it = gw; it < NIT; it += NGW) {
;           const WItem nxt = decode(it + NGW); witem_load(nxt, vn);
;           __builtin_amdgcn_sched_barrier(0);
;           witem_store(cur, v);
;           __builtin_amdgcn_sched_barrier(0);
; #pragma unroll
;           for (int i = 0; i < 16; ++i) v[i] = vn[i];
;           cur = nxt; } }
.LBB0_1880:
.Lcn_left:
	s_and_b32 s8, s101, 0x3fffffff
	s_cmp_ge_u32 s8, 168
	s_cbranch_scc1 .Lcn_leftdone
	s_and_b32 s8, s101, 0x3fffffff
	s_cmp_ge_u32 s8, 168
	s_cbranch_scc1 .Lcn_ldum_lfA
	s_and_b32 s8, s101, 0x3fffffff
	s_mul_i32 s9, s8, 0x2493
	s_lshr_b32 s9, s9, 16
	s_mul_i32 s10, s9, 7
	s_sub_u32 s10, s8, s10
	s_lshl_b32 s10, s10, 8
	s_lshr_b32 s11, s100, 3
	s_add_u32 s10, s10, s11
	s_and_b32 s8, s100, 7
	s_cmp_ge_u32 s9, 16
	s_cbranch_scc1 .Lcn_dn_lfAs
	s_lshr_b32 s11, s10, 4
	s_mul_i32 s11, s11, 0x2493
	s_lshr_b32 s11, s11, 16
	s_mul_i32 s12, s11, 0x70
	s_sub_u32 s12, s10, s12
	s_lshr_b32 s10, s8, 1
	s_lshl_b32 s11, s11, 2
	s_add_u32 s11, s11, s10
	s_and_b32 s8, s8, 1
	s_lshl_b32 s12, s12, 1
	s_add_u32 s12, s12, s8
	s_and_b32 s10, s9, 1
	s_lshr_b32 s9, s9, 1
	s_mul_i32 s8, s9, 0x3800000
	s_mul_i32 s9, s11, 0xe0000
	s_add_u32 s8, s8, s9
	s_lshl_b32 s9, s12, 7
	s_add_u32 s8, s8, s9
	v_readlane_b32 s32, v255, 46
	v_readlane_b32 s33, v255, 47
	s_cmp_eq_u32 s10, 0
	s_cselect_b32 s32, s98, s32
	s_cselect_b32 s33, s99, s33
	s_add_u32 s32, s32, s8
	s_addc_u32 s33, s33, 0
	s_movk_i32 s1, 0x7000
	s_branch .Lcn_dd_lfAs
.Lcn_dn_lfAs:
	s_sub_u32 s9, s9, 16
	s_lshr_b32 s11, s10, 5
	s_and_b32 s12, s10, 31
	s_lshr_b32 s10, s8, 1
	s_lshl_b32 s11, s11, 2
	s_add_u32 s11, s11, s10
	s_and_b32 s8, s8, 1
	s_lshl_b32 s12, s12, 1
	s_add_u32 s12, s12, s8
	s_mul_i32 s8, s9, 0x3800000
	s_lshl_b32 s9, s11, 18
	s_add_u32 s8, s8, s9
	s_lshl_b32 s9, s12, 7
	s_add_u32 s8, s8, s9
	v_readlane_b32 s32, v255, 48
	v_readlane_b32 s33, v255, 49
	s_add_u32 s32, s32, s8
	s_addc_u32 s33, s33, 0
	s_movk_i32 s1, 0x2000

; __device__ __forceinline__ void witem_load(const WItem& w, f32x4 (&v)[16]) {
;     if (!w.valid) return;
; #pragma unroll
;     for (int i = 0; i < 16; ++i) v[i] = *(const f32x4*)(w.src + (size_t)i * w.N);
; }
; __device__ __forceinline__ void p0_weights(const Args& a, LAS unsigned char* lds) {
;     ...
;         else if ((r -= I_FD) < 16 * I_MG) { const int up = r / (8 * I_MG); r -= up * 8 * I_MG; const int e = r / I_MG; r -= e * I_MG; W = a.in[up ? I_MWU : I_MWG] + (size_t)e * D * DFE; w.K = D; w.N = DFE;
;             w.dst = a.ws + WS_MGU_T + (size_t)e * 2 * DFE * D * (MOE_FP8 ? 1 : 2); w.kind = 2 + up; w.f8 = MOE_FP8; w.scale = F8_WGU; }
;         else { r -= 16 * I_MG; const int e = r / I_MD; r -= e * I_MD; W = a.in[I_MWD] + (size_t)e * DFE * D; w.K = DFE; w.N = D; w.dst = a.ws + WS_MD_T + (size_t)e * D * DFE * (MOE_FP8 ? 1 : 2); w.f8 = MOE_FP8; w.scale = F8_WD; }
;         const int nblk = (w.N + 31) >> 5, kb = r / nblk, nb = r - kb * nblk;
;         w.k0 = 128 * kb + 16 * (lane >> 3); w.n = 32 * nb + 4 * (lane & 7); w.valid = w.n < w.N; w.src = W + (size_t)w.k0 * w.N + w.n;
.Lcn_lgo_lfA:
	v_and_b32_e32 v112, 63, v0
	v_and_b32_e32 v114, 7, v112
	v_lshrrev_b32_e32 v112, 3, v112
	v_lshlrev_b32_e32 v112, 2, v112
	v_lshlrev_b32_e32 v113, 4, v114
	v_lshlrev_b32_e32 v114, 2, v114
	v_mad_u32_u24 v115, v112, s1, v113
	global_load_dwordx4 v[100:103], v115, s[32:33] nt
	s_add_u32 s32, s32, s1
	s_addc_u32 s33, s33, 0
	global_load_dwordx4 v[104:107], v115, s[32:33] nt
	s_add_u32 s32, s32, s1
	s_addc_u32 s33, s33, 0
	global_load_dwordx4 v[108:111], v115, s[32:33] nt
	s_add_u32 s32, s32, s1
	s_addc_u32 s33, s33, 0
	global_load_dwordx4 v[112:115], v115, s[32:33] nt
	s_and_b32 s8, s101, 0x3fffffff
	s_cmp_ge_u32 s8, 168
	s_cbranch_scc1 .Lcn_ldum_lfB
	s_and_b32 s8, s101, 0x3fffffff
	s_mul_i32 s9, s8, 0x2493
	s_lshr_b32 s9, s9, 16
	s_mul_i32 s10, s9, 7
	s_sub_u32 s10, s8, s10
	s_lshl_b32 s10, s10, 8
	s_lshr_b32 s11, s100, 3
	s_add_u32 s10, s10, s11
	s_and_b32 s8, s100, 7
	s_cmp_ge_u32 s9, 16
	s_cbranch_scc1 .Lcn_dn_lfBs
	s_lshr_b32 s11, s10, 4
	s_mul_i32 s11, s11, 0x2493
	s_lshr_b32 s11, s11, 16
	s_mul_i32 s12, s11, 0x70
	s_sub_u32 s12, s10, s12
	s_lshr_b32 s10, s8, 1
	s_lshl_b32 s11, s11, 2
	s_add_u32 s11, s11, s10
	s_and_b32 s8, s8, 1
	s_lshl_b32 s12, s12, 1
	s_add_u32 s12, s12, s8
	s_and_b32 s10, s9, 1
	s_lshr_b32 s9, s9, 1
	s_mul_i32 s8, s9, 0x3800000
	s_mul_i32 s9, s11, 0xe0000
	s_add_u32 s8, s8, s9
	s_lshl_b32 s9, s12, 7
	s_add_u32 s8, s8, s9
	v_readlane_b32 s32, v255, 46
	v_readlane_b32 s33, v255, 47
	s_cmp_eq_u32 s10, 0
	s_cselect_b32 s32, s98, s32
	s_cselect_b32 s33, s99, s33
	s_add_u32 s32, s32, s8
	s_addc_u32 s33, s33, 0
	s_movk_i32 s1, 0x7000
	s_branch .Lcn_dd_lfBs

; __device__ __forceinline__ void witem_load(const WItem& w, f32x4 (&v)[16]) {
;     if (!w.valid) return;
; #pragma unroll
;     for (int i = 0; i < 16; ++i) v[i] = *(const f32x4*)(w.src + (size_t)i * w.N);
; }
; __device__ __forceinline__ void p0_weights(const Args& a, LAS unsigned char* lds) {
;     ...
;         else if ((r -= I_FD) < 16 * I_MG) { const int up = r / (8 * I_MG); r -= up * 8 * I_MG; const int e = r / I_MG; r -= e * I_MG; W = a.in[up ? I_MWU : I_MWG] + (size_t)e * D * DFE; w.K = D; w.N = DFE;
;             w.dst = a.ws + WS_MGU_T + (size_t)e * 2 * DFE * D * (MOE_FP8 ? 1 : 2); w.kind = 2 + up; w.f8 = MOE_FP8; w.scale = F8_WGU; }
;         else { r -= 16 * I_MG; const int e = r / I_MD; r -= e * I_MD; W = a.in[I_MWD] + (size_t)e * DFE * D; w.K = DFE; w.N = D; w.dst = a.ws + WS_MD_T + (size_t)e * D * DFE * (MOE_FP8 ? 1 : 2); w.f8 = MOE_FP8; w.scale = F8_WD; }
;         const int nblk = (w.N + 31) >> 5, kb = r / nblk, nb = r - kb * nblk;
;         w.k0 = 128 * kb + 16 * (lane >> 3); w.n = 32 * nb + 4 * (lane & 7); w.valid = w.n < w.N; w.src = W + (size_t)w.k0 * w.N + w.n;
.Lcn_dd_lfBs:
	s_and_b32 s26, s101, 0x3fffffff
	s_bitset1_b32 s26, 31
	s_add_u32 s101, s101, 1
	s_branch .Lcn_lgo_lfB
.Lcn_ldum_lfB:
	v_readlane_b32 s32, v255, 52
	v_readlane_b32 s33, v255, 53
	s_add_u32 s32, s32, 0x500000
	s_addc_u32 s33, s33, 0
	s_movk_i32 s1, 0x2000
	s_mov_b32 s26, 0
.Lcn_lgo_lfB:
	v_and_b32_e32 v128, 63, v0
	v_and_b32_e32 v130, 7, v128
	v_lshrrev_b32_e32 v128, 3, v128
	v_lshlrev_b32_e32 v128, 2, v128
	v_lshlrev_b32_e32 v129, 4, v130
	v_lshlrev_b32_e32 v130, 2, v130
	v_mad_u32_u24 v131, v128, s1, v129
	global_load_dwordx4 v[116:119], v131, s[32:33] nt
	s_add_u32 s32, s32, s1
	s_addc_u32 s33, s33, 0
	global_load_dwordx4 v[120:123], v131, s[32:33] nt
	s_add_u32 s32, s32, s1
	s_addc_u32 s33, s33, 0
	global_load_dwordx4 v[124:127], v131, s[32:33] nt
	s_add_u32 s32, s32, s1
	s_addc_u32 s33, s33, 0
	global_load_dwordx4 v[128:131], v131, s[32:33] nt
	s_and_b32 s8, s101, 0x3fffffff
	s_cmp_ge_u32 s8, 168
	s_cbranch_scc1 .Lcn_ldum_lfC
	s_and_b32 s8, s101, 0x3fffffff
	s_mul_i32 s9, s8, 0x2493
	s_lshr_b32 s9, s9, 16
	s_mul_i32 s10, s9, 7
	s_sub_u32 s10, s8, s10
	s_lshl_b32 s10, s10, 8
	s_lshr_b32 s11, s100, 3
	s_add_u32 s10, s10, s11
	s_and_b32 s8, s100, 7
	s_cmp_ge_u32 s9, 16
	s_cbranch_scc1 .Lcn_dn_lfCs
	s_lshr_b32 s11, s10, 4
	s_mul_i32 s11, s11, 0x2493
	s_lshr_b32 s11, s11, 16
	s_mul_i32 s12, s11, 0x70
	s_sub_u32 s12, s10, s12
	s_lshr_b32 s10, s8, 1
	s_lshl_b32 s11, s11, 2
	s_add_u32 s11, s11, s10
	s_and_b32 s8, s8, 1
	s_lshl_b32 s12, s12, 1
	s_add_u32 s12, s12, s8
	s_and_b32 s10, s9, 1
	s_lshr_b32 s9, s9, 1
	s_mul_i32 s8, s9, 0x3800000
	s_mul_i32 s9, s11, 0xe0000
	s_add_u32 s8, s8, s9
	s_lshl_b32 s9, s12, 7
	s_add_u32 s8, s8, s9
	v_readlane_b32 s32, v255, 46
	v_readlane_b32 s33, v255, 47
	s_cmp_eq_u32 s10, 0
	s_cselect_b32 s32, s98, s32
	s_cselect_b32 s33, s99, s33
	s_add_u32 s32, s32, s8
	s_addc_u32 s33, s33, 0
	s_movk_i32 s1, 0x7000
	s_branch .Lcn_dd_lfCs

; __device__ __forceinline__ void witem_load(const WItem& w, f32x4 (&v)[16]) {
;     if (!w.valid) return;
; #pragma unroll
;     for (int i = 0; i < 16; ++i) v[i] = *(const f32x4*)(w.src + (size_t)i * w.N);
; }
; __device__ __forceinline__ void p0_weights(const Args& a, LAS unsigned char* lds) {
;     ...
;         else if ((r -= I_FD) < 16 * I_MG) { const int up = r / (8 * I_MG); r -= up * 8 * I_MG; const int e = r / I_MG; r -= e * I_MG; W = a.in[up ? I_MWU : I_MWG] + (size_t)e * D * DFE; w.K = D; w.N = DFE;
;             w.dst = a.ws + WS_MGU_T + (size_t)e * 2 * DFE * D * (MOE_FP8 ? 1 : 2); w.kind = 2 + up; w.f8 = MOE_FP8; w.scale = F8_WGU; }
;         else { r -= 16 * I_MG; const int e = r / I_MD; r -= e * I_MD; W = a.in[I_MWD] + (size_t)e * DFE * D; w.K = DFE; w.N = D; w.dst = a.ws + WS_MD_T + (size_t)e * D * DFE * (MOE_FP8 ? 1 : 2); w.f8 = MOE_FP8; w.scale = F8_WD; }
;         const int nblk = (w.N + 31) >> 5, kb = r / nblk, nb = r - kb * nblk;
;         w.k0 = 128 * kb + 16 * (lane >> 3); w.n = 32 * nb + 4 * (lane & 7); w.valid = w.n < w.N; w.src = W + (size_t)w.k0 * w.N + w.n;
.Lcn_dd_lfCs:
	s_and_b32 s27, s101, 0x3fffffff
	s_bitset1_b32 s27, 31
	s_add_u32 s101, s101, 1
	s_branch .Lcn_lgo_lfC
.Lcn_ldum_lfC:
	v_readlane_b32 s32, v255, 52
	v_readlane_b32 s33, v255, 53
	s_add_u32 s32, s32, 0x500000
	s_addc_u32 s33, s33, 0
	s_movk_i32 s1, 0x2000
	s_mov_b32 s27, 0
.Lcn_lgo_lfC:
	v_and_b32_e32 v144, 63, v0
	v_and_b32_e32 v146, 7, v144
	v_lshrrev_b32_e32 v144, 3, v144
	v_lshlrev_b32_e32 v144, 2, v144
	v_lshlrev_b32_e32 v145, 4, v146
	v_lshlrev_b32_e32 v146, 2, v146
	v_mad_u32_u24 v147, v144, s1, v145
	global_load_dwordx4 v[132:135], v147, s[32:33] nt
	s_add_u32 s32, s32, s1
	s_addc_u32 s33, s33, 0
	global_load_dwordx4 v[136:139], v147, s[32:33] nt
	s_add_u32 s32, s32, s1
	s_addc_u32 s33, s33, 0
	global_load_dwordx4 v[140:143], v147, s[32:33] nt
	s_add_u32 s32, s32, s1
	s_addc_u32 s33, s33, 0
	global_load_dwordx4 v[144:147], v147, s[32:33] nt
	s_and_b32 s8, s101, 0x3fffffff
	s_cmp_ge_u32 s8, 168
	s_cbranch_scc1 .Lcn_ldum_lfD
	s_and_b32 s8, s101, 0x3fffffff
	s_mul_i32 s9, s8, 0x2493
	s_lshr_b32 s9, s9, 16
	s_mul_i32 s10, s9, 7
	s_sub_u32 s10, s8, s10
	s_lshl_b32 s10, s10, 8
	s_lshr_b32 s11, s100, 3
	s_add_u32 s10, s10, s11
	s_and_b32 s8, s100, 7
	s_cmp_ge_u32 s9, 16
	s_cbranch_scc1 .Lcn_dn_lfDs
	s_lshr_b32 s11, s10, 4
	s_mul_i32 s11, s11, 0x2493
	s_lshr_b32 s11, s11, 16
	s_mul_i32 s12, s11, 0x70
	s_sub_u32 s12, s10, s12
	s_lshr_b32 s10, s8, 1
	s_lshl_b32 s11, s11, 2
	s_add_u32 s11, s11, s10
	s_and_b32 s8, s8, 1
	s_lshl_b32 s12, s12, 1
	s_add_u32 s12, s12, s8
	s_and_b32 s10, s9, 1
	s_lshr_b32 s9, s9, 1
	s_mul_i32 s8, s9, 0x3800000
	s_mul_i32 s9, s11, 0xe0000
	s_add_u32 s8, s8, s9
	s_lshl_b32 s9, s12, 7
	s_add_u32 s8, s8, s9
	v_readlane_b32 s32, v255, 46
	v_readlane_b32 s33, v255, 47
	s_cmp_eq_u32 s10, 0
	s_cselect_b32 s32, s98, s32
	s_cselect_b32 s33, s99, s33
	s_add_u32 s32, s32, s8
	s_addc_u32 s33, s33, 0
	s_movk_i32 s1, 0x7000
	s_branch .Lcn_dd_lfDs

; __device__ __forceinline__ unsigned pk4_fp8(float a, float b, float c, float d) { int p = __builtin_amdgcn_cvt_pk_fp8_f32(a, b, 0, false); p = __builtin_amdgcn_cvt_pk_fp8_f32(c, d, p, true); return (unsigned)p; }
; __device__ __forceinline__ void witem_store(const WItem& w, const f32x4 (&v)[16]) {
;     if (!w.valid) return;
;     if (w.f8) {
; #pragma unroll
;         for (int j = 0; j < 4; ++j) { u32x4 o; const float sc = w.scale;
;             o.x = pk4_fp8(v[0][j] * sc, v[1][j] * sc, v[2][j] * sc, v[3][j] * sc); o.y = pk4_fp8(v[4][j] * sc, v[5][j] * sc, v[6][j] * sc, v[7][j] * sc);
;             o.z = pk4_fp8(v[8][j] * sc, v[9][j] * sc, v[10][j] * sc, v[11][j] * sc); o.w = pk4_fp8(v[12][j] * sc, v[13][j] * sc, v[14][j] * sc, v[15][j] * sc);
;             *(u32x4*)(w.dst + (size_t)witem_row(w.kind, w.n + j) * w.K + w.k0) = o; }
; __device__ __forceinline__ void p0_weights(const Args& a, LAS unsigned char* lds) {
;     ...
;         else if ((r -= I_FD) < 16 * I_MG) { const int up = r / (8 * I_MG); r -= up * 8 * I_MG; const int e = r / I_MG; r -= e * I_MG; W = a.in[up ? I_MWU : I_MWG] + (size_t)e * D * DFE; w.K = D; w.N = DFE;
;             w.dst = a.ws + WS_MGU_T + (size_t)e * 2 * DFE * D * (MOE_FP8 ? 1 : 2); w.kind = 2 + up; w.f8 = MOE_FP8; w.scale = F8_WGU; }
;         else { r -= 16 * I_MG; const int e = r / I_MD; r -= e * I_MD; W = a.in[I_MWD] + (size_t)e * DFE * D; w.K = DFE; w.N = D; w.dst = a.ws + WS_MD_T + (size_t)e * D * DFE * (MOE_FP8 ? 1 : 2); w.f8 = MOE_FP8; w.scale = F8_WD; }
;         const int nblk = (w.N + 31) >> 5, kb = r / nblk, nb = r - kb * nblk;
;         w.k0 = 128 * kb + 16 * (lane >> 3); w.n = 32 * nb + 4 * (lane & 7); w.valid = w.n < w.N; w.src = W + (size_t)w.k0 * w.N + w.n;
.Lcn_dd_lfDs:
	s_and_b32 s28, s101, 0x3fffffff
	s_bitset1_b32 s28, 31
	s_add_u32 s101, s101, 1
	s_branch .Lcn_lgo_lfD
.Lcn_ldum_lfD:
	v_readlane_b32 s32, v255, 52
	v_readlane_b32 s33, v255, 53
	s_add_u32 s32, s32, 0x500000
	s_addc_u32 s33, s33, 0
	s_movk_i32 s1, 0x2000
	s_mov_b32 s28, 0
.Lcn_lgo_lfD:
	v_and_b32_e32 v160, 63, v0
	v_and_b32_e32 v162, 7, v160
	v_lshrrev_b32_e32 v160, 3, v160
	v_lshlrev_b32_e32 v160, 2, v160
	v_lshlrev_b32_e32 v161, 4, v162
	v_lshlrev_b32_e32 v162, 2, v162
	v_mad_u32_u24 v163, v160, s1, v161
	global_load_dwordx4 v[148:151], v163, s[32:33] nt
	s_add_u32 s32, s32, s1
	s_addc_u32 s33, s33, 0
	global_load_dwordx4 v[152:155], v163, s[32:33] nt
	s_add_u32 s32, s32, s1
	s_addc_u32 s33, s33, 0
	global_load_dwordx4 v[156:159], v163, s[32:33] nt
	s_add_u32 s32, s32, s1
	s_addc_u32 s33, s33, 0
	global_load_dwordx4 v[160:163], v163, s[32:33] nt
	s_waitcnt vmcnt(0)
	s_bitset0_b32 s101, 30
	s_bitcmp1_b32 s25, 31
	s_cbranch_scc0 .Lcn_snone_lfA
	s_and_b32 s8, s25, 0x3fffffff
	s_mul_i32 s9, s8, 0x2493
	s_lshr_b32 s9, s9, 16
	s_mul_i32 s10, s9, 7
	s_sub_u32 s10, s8, s10
	s_lshl_b32 s10, s10, 8
	s_lshr_b32 s11, s100, 3
	s_add_u32 s10, s10, s11
	s_and_b32 s8, s100, 7
	s_cmp_ge_u32 s9, 16
	s_cbranch_scc1 .Lcn_dn_lfAd
	s_lshr_b32 s11, s10, 4
	s_mul_i32 s11, s11, 0x2493
	s_lshr_b32 s11, s11, 16
	s_mul_i32 s12, s11, 0x70
	s_sub_u32 s12, s10, s12
	s_lshr_b32 s10, s8, 1
	s_lshl_b32 s11, s11, 2
	s_add_u32 s11, s11, s10
	s_and_b32 s8, s8, 1
	s_lshl_b32 s12, s12, 1
	s_add_u32 s12, s12, s8
	s_and_b32 s10, s9, 1
	s_lshr_b32 s9, s9, 1
	s_mul_i32 s8, s9, 0x1c00000
	s_add_u32 s8, s8, 0x4a000000
	s_lshr_b32 s9, s12, 2
	s_lshl_b32 s9, s9, 8
	s_lshl_b32 s10, s10, 7
	s_add_u32 s9, s9, s10
	s_and_b32 s10, s12, 3
	s_lshl_b32 s10, s10, 5
	s_add_u32 s9, s9, s10
	s_lshl_b32 s9, s9, 11
	s_add_u32 s8, s8, s9
	s_lshl_b32 s9, s11, 5
	s_add_u32 s8, s8, s9
	v_readlane_b32 s32, v255, 52
	v_readlane_b32 s33, v255, 53
	s_add_u32 s32, s32, s8
	s_addc_u32 s33, s33, 0
	s_movk_i32 s1, 0x800
	s_mov_b32 s0, 0x42000000
	s_branch .Lcn_dd_lfAd
.Lcn_dn_lfAd:
	s_sub_u32 s9, s9, 16
	s_lshr_b32 s11, s10, 5
	s_and_b32 s12, s10, 31
	s_lshr_b32 s10, s8, 1
	s_lshl_b32 s11, s11, 2
	s_add_u32 s11, s11, s10
	s_and_b32 s8, s8, 1
	s_lshl_b32 s12, s12, 1
	s_add_u32 s12, s12, s8
	s_mul_i32 s8, s9, 0xe00000
	s_add_u32 s8, s8, 0x66000000
	s_mul_i32 s9, s12, 0x38000
	s_add_u32 s8, s8, s9
	s_lshl_b32 s9, s11, 5
	s_add_u32 s8, s8, s9
	v_readlane_b32 s32, v255, 52
	v_readlane_b32 s33, v255, 53
	s_add_u32 s32, s32, s8
	s_addc_u32 s33, s33, 0
	s_movk_i32 s1, 0x1c00
	s_mov_b32 s0, 0x43000000
.Lcn_dd_lfAd:
	s_mov_b32 s25, 0
	s_bitset1_b32 s101, 30
	v_mul_f32_e32 v100, s0, v100
	v_mul_f32_e32 v101, s0, v101
	v_mul_f32_e32 v102, s0, v102
	v_mul_f32_e32 v103, s0, v103
	v_mul_f32_e32 v104, s0, v104
	v_mul_f32_e32 v105, s0, v105
	v_mul_f32_e32 v106, s0, v106
	v_mul_f32_e32 v107, s0, v107
	v_mul_f32_e32 v108, s0, v108
	v_mul_f32_e32 v109, s0, v109
	v_mul_f32_e32 v110, s0, v110
	v_mul_f32_e32 v111, s0, v111
	v_mul_f32_e32 v112, s0, v112
	v_mul_f32_e32 v113, s0, v113
	v_mul_f32_e32 v114, s0, v114
	v_mul_f32_e32 v115, s0, v115
	v_cvt_pk_fp8_f32 v100, v100, v104
	v_cvt_pk_fp8_f32 v101, v101, v105
	v_cvt_pk_fp8_f32 v102, v102, v106
	v_cvt_pk_fp8_f32 v103, v103, v107
	v_cvt_pk_fp8_f32 v100, v108, v112 op_sel:[0,0,1]
	v_cvt_pk_fp8_f32 v101, v109, v113 op_sel:[0,0,1]
	v_cvt_pk_fp8_f32 v102, v110, v114 op_sel:[0,0,1]
	v_cvt_pk_fp8_f32 v103, v111, v115 op_sel:[0,0,1]
	v_and_b32_e32 v104, 63, v0
	v_and_b32_e32 v106, 7, v104
	v_lshrrev_b32_e32 v104, 3, v104
	v_lshlrev_b32_e32 v104, 2, v104
	v_lshlrev_b32_e32 v105, 4, v106
	v_lshlrev_b32_e32 v106, 2, v106
	v_mad_u32_u24 v105, v106, s1, v104
	global_store_dword v105, v100, s[32:33] nt
	v_add_u32_e32 v104, s1, v105
	global_store_dword v104, v101, s[32:33] nt
	v_add_u32_e32 v106, s1, v104
	global_store_dword v106, v102, s[32:33] nt
	v_add_u32_e32 v107, s1, v106
	global_store_dword v107, v103, s[32:33] nt
.Lcn_snone_lfA:
	s_bitset0_b32 s101, 30
	s_bitcmp1_b32 s26, 31
	s_cbranch_scc0 .Lcn_snone_lfB
	s_and_b32 s8, s26, 0x3fffffff
	s_mul_i32 s9, s8, 0x2493
	s_lshr_b32 s9, s9, 16
	s_mul_i32 s10, s9, 7
	s_sub_u32 s10, s8, s10
	s_lshl_b32 s10, s10, 8
	s_lshr_b32 s11, s100, 3
	s_add_u32 s10, s10, s11
	s_and_b32 s8, s100, 7
	s_cmp_ge_u32 s9, 16
	s_cbranch_scc1 .Lcn_dn_lfBd
	s_lshr_b32 s11, s10, 4
	s_mul_i32 s11, s11, 0x2493
	s_lshr_b32 s11, s11, 16
	s_mul_i32 s12, s11, 0x70
	s_sub_u32 s12, s10, s12
	s_lshr_b32 s10, s8, 1
	s_lshl_b32 s11, s11, 2
	s_add_u32 s11, s11, s10
	s_and_b32 s8, s8, 1
	s_lshl_b32 s12, s12, 1
	s_add_u32 s12, s12, s8
	s_and_b32 s10, s9, 1
	s_lshr_b32 s9, s9, 1
	s_mul_i32 s8, s9, 0x1c00000
	s_add_u32 s8, s8, 0x4a000000
	s_lshr_b32 s9, s12, 2
	s_lshl_b32 s9, s9, 8
	s_lshl_b32 s10, s10, 7
	s_add_u32 s9, s9, s10
	s_and_b32 s10, s12, 3
	s_lshl_b32 s10, s10, 5
	s_add_u32 s9, s9, s10
	s_lshl_b32 s9, s9, 11
	s_add_u32 s8, s8, s9
	s_lshl_b32 s9, s11, 5
	s_add_u32 s8, s8, s9
	v_readlane_b32 s32, v255, 52
	v_readlane_b32 s33, v255, 53
	s_add_u32 s32, s32, s8
	s_addc_u32 s33, s33, 0
	s_movk_i32 s1, 0x800
	s_mov_b32 s0, 0x42000000
	s_branch .Lcn_dd_lfBd

; __device__ __forceinline__ unsigned pk4_fp8(float a, float b, float c, float d) { int p = __builtin_amdgcn_cvt_pk_fp8_f32(a, b, 0, false); p = __builtin_amdgcn_cvt_pk_fp8_f32(c, d, p, true); return (unsigned)p; }
; __device__ __forceinline__ void witem_store(const WItem& w, const f32x4 (&v)[16]) {
;     if (!w.valid) return;
;     if (w.f8) {
; #pragma unroll
;         for (int j = 0; j < 4; ++j) { u32x4 o; const float sc = w.scale;
;             o.x = pk4_fp8(v[0][j] * sc, v[1][j] * sc, v[2][j] * sc, v[3][j] * sc); o.y = pk4_fp8(v[4][j] * sc, v[5][j] * sc, v[6][j] * sc, v[7][j] * sc);
;             o.z = pk4_fp8(v[8][j] * sc, v[9][j] * sc, v[10][j] * sc, v[11][j] * sc); o.w = pk4_fp8(v[12][j] * sc, v[13][j] * sc, v[14][j] * sc, v[15][j] * sc);
;             *(u32x4*)(w.dst + (size_t)witem_row(w.kind, w.n + j) * w.K + w.k0) = o; }
; __device__ __forceinline__ void p0_weights(const Args& a, LAS unsigned char* lds) {
;     ...
;         else if ((r -= I_FD) < 16 * I_MG) { const int up = r / (8 * I_MG); r -= up * 8 * I_MG; const int e = r / I_MG; r -= e * I_MG; W = a.in[up ? I_MWU : I_MWG] + (size_t)e * D * DFE; w.K = D; w.N = DFE;
;             w.dst = a.ws + WS_MGU_T + (size_t)e * 2 * DFE * D * (MOE_FP8 ? 1 : 2); w.kind = 2 + up; w.f8 = MOE_FP8; w.scale = F8_WGU; }
;         else { r -= 16 * I_MG; const int e = r / I_MD; r -= e * I_MD; W = a.in[I_MWD] + (size_t)e * DFE * D; w.K = DFE; w.N = D; w.dst = a.ws + WS_MD_T + (size_t)e * D * DFE * (MOE_FP8 ? 1 : 2); w.f8 = MOE_FP8; w.scale = F8_WD; }
;         const int nblk = (w.N + 31) >> 5, kb = r / nblk, nb = r - kb * nblk;
;         w.k0 = 128 * kb + 16 * (lane >> 3); w.n = 32 * nb + 4 * (lane & 7); w.valid = w.n < w.N; w.src = W + (size_t)w.k0 * w.N + w.n;
.Lcn_dd_lfBd:
	s_mov_b32 s26, 0
	s_bitset1_b32 s101, 30
	v_mul_f32_e32 v116, s0, v116
	v_mul_f32_e32 v117, s0, v117
	v_mul_f32_e32 v118, s0, v118
	v_mul_f32_e32 v119, s0, v119
	v_mul_f32_e32 v120, s0, v120
	v_mul_f32_e32 v121, s0, v121
	v_mul_f32_e32 v122, s0, v122
	v_mul_f32_e32 v123, s0, v123
	v_mul_f32_e32 v124, s0, v124
	v_mul_f32_e32 v125, s0, v125
	v_mul_f32_e32 v126, s0, v126
	v_mul_f32_e32 v127, s0, v127
	v_mul_f32_e32 v128, s0, v128
	v_mul_f32_e32 v129, s0, v129
	v_mul_f32_e32 v130, s0, v130
	v_mul_f32_e32 v131, s0, v131
	v_cvt_pk_fp8_f32 v116, v116, v120
	v_cvt_pk_fp8_f32 v117, v117, v121
	v_cvt_pk_fp8_f32 v118, v118, v122
	v_cvt_pk_fp8_f32 v119, v119, v123
	v_cvt_pk_fp8_f32 v116, v124, v128 op_sel:[0,0,1]
	v_cvt_pk_fp8_f32 v117, v125, v129 op_sel:[0,0,1]
	v_cvt_pk_fp8_f32 v118, v126, v130 op_sel:[0,0,1]
	v_cvt_pk_fp8_f32 v119, v127, v131 op_sel:[0,0,1]
	v_and_b32_e32 v120, 63, v0
	v_and_b32_e32 v122, 7, v120
	v_lshrrev_b32_e32 v120, 3, v120
	v_lshlrev_b32_e32 v120, 2, v120
	v_lshlrev_b32_e32 v121, 4, v122
	v_lshlrev_b32_e32 v122, 2, v122
	v_mad_u32_u24 v121, v122, s1, v120
	global_store_dword v121, v116, s[32:33] nt
	v_add_u32_e32 v120, s1, v121
	global_store_dword v120, v117, s[32:33] nt
	v_add_u32_e32 v122, s1, v120
	global_store_dword v122, v118, s[32:33] nt
	v_add_u32_e32 v123, s1, v122
	global_store_dword v123, v119, s[32:33] nt
.Lcn_snone_lfB:
	s_bitset0_b32 s101, 30
	s_bitcmp1_b32 s27, 31
	s_cbranch_scc0 .Lcn_snone_lfC
	s_and_b32 s8, s27, 0x3fffffff
	s_mul_i32 s9, s8, 0x2493
	s_lshr_b32 s9, s9, 16
	s_mul_i32 s10, s9, 7
	s_sub_u32 s10, s8, s10
	s_lshl_b32 s10, s10, 8
	s_lshr_b32 s11, s100, 3
	s_add_u32 s10, s10, s11
	s_and_b32 s8, s100, 7
	s_cmp_ge_u32 s9, 16
	s_cbranch_scc1 .Lcn_dn_lfCd
	s_lshr_b32 s11, s10, 4
	s_mul_i32 s11, s11, 0x2493
	s_lshr_b32 s11, s11, 16
	s_mul_i32 s12, s11, 0x70
	s_sub_u32 s12, s10, s12
	s_lshr_b32 s10, s8, 1
	s_lshl_b32 s11, s11, 2
	s_add_u32 s11, s11, s10
	s_and_b32 s8, s8, 1
	s_lshl_b32 s12, s12, 1
	s_add_u32 s12, s12, s8
	s_and_b32 s10, s9, 1
	s_lshr_b32 s9, s9, 1
	s_mul_i32 s8, s9, 0x1c00000
	s_add_u32 s8, s8, 0x4a000000
	s_lshr_b32 s9, s12, 2
	s_lshl_b32 s9, s9, 8
	s_lshl_b32 s10, s10, 7
	s_add_u32 s9, s9, s10
	s_and_b32 s10, s12, 3
	s_lshl_b32 s10, s10, 5
	s_add_u32 s9, s9, s10
	s_lshl_b32 s9, s9, 11
	s_add_u32 s8, s8, s9
	s_lshl_b32 s9, s11, 5
	s_add_u32 s8, s8, s9
	v_readlane_b32 s32, v255, 52
	v_readlane_b32 s33, v255, 53
	s_add_u32 s32, s32, s8
	s_addc_u32 s33, s33, 0
	s_movk_i32 s1, 0x800
	s_mov_b32 s0, 0x42000000
	s_branch .Lcn_dd_lfCd

; __device__ __forceinline__ unsigned pk4_fp8(float a, float b, float c, float d) { int p = __builtin_amdgcn_cvt_pk_fp8_f32(a, b, 0, false); p = __builtin_amdgcn_cvt_pk_fp8_f32(c, d, p, true); return (unsigned)p; }
; __device__ __forceinline__ void witem_store(const WItem& w, const f32x4 (&v)[16]) {
;     if (!w.valid) return;
;     if (w.f8) {
; #pragma unroll
;         for (int j = 0; j < 4; ++j) { u32x4 o; const float sc = w.scale;
;             o.x = pk4_fp8(v[0][j] * sc, v[1][j] * sc, v[2][j] * sc, v[3][j] * sc); o.y = pk4_fp8(v[4][j] * sc, v[5][j] * sc, v[6][j] * sc, v[7][j] * sc);
;             o.z = pk4_fp8(v[8][j] * sc, v[9][j] * sc, v[10][j] * sc, v[11][j] * sc); o.w = pk4_fp8(v[12][j] * sc, v[13][j] * sc, v[14][j] * sc, v[15][j] * sc);
;             *(u32x4*)(w.dst + (size_t)witem_row(w.kind, w.n + j) * w.K + w.k0) = o; }
; __device__ __forceinline__ void p0_weights(const Args& a, LAS unsigned char* lds) {
;     ...
;         else if ((r -= I_FD) < 16 * I_MG) { const int up = r / (8 * I_MG); r -= up * 8 * I_MG; const int e = r / I_MG; r -= e * I_MG; W = a.in[up ? I_MWU : I_MWG] + (size_t)e * D * DFE; w.K = D; w.N = DFE;
;             w.dst = a.ws + WS_MGU_T + (size_t)e * 2 * DFE * D * (MOE_FP8 ? 1 : 2); w.kind = 2 + up; w.f8 = MOE_FP8; w.scale = F8_WGU; }
;         else { r -= 16 * I_MG; const int e = r / I_MD; r -= e * I_MD; W = a.in[I_MWD] + (size_t)e * DFE * D; w.K = DFE; w.N = D; w.dst = a.ws + WS_MD_T + (size_t)e * D * DFE * (MOE_FP8 ? 1 : 2); w.f8 = MOE_FP8; w.scale = F8_WD; }
;         const int nblk = (w.N + 31) >> 5, kb = r / nblk, nb = r - kb * nblk;
;         w.k0 = 128 * kb + 16 * (lane >> 3); w.n = 32 * nb + 4 * (lane & 7); w.valid = w.n < w.N; w.src = W + (size_t)w.k0 * w.N + w.n;
.Lcn_dd_lfCd:
	s_mov_b32 s27, 0
	s_bitset1_b32 s101, 30
	v_mul_f32_e32 v132, s0, v132
	v_mul_f32_e32 v133, s0, v133
	v_mul_f32_e32 v134, s0, v134
	v_mul_f32_e32 v135, s0, v135
	v_mul_f32_e32 v136, s0, v136
	v_mul_f32_e32 v137, s0, v137
	v_mul_f32_e32 v138, s0, v138
	v_mul_f32_e32 v139, s0, v139
	v_mul_f32_e32 v140, s0, v140
	v_mul_f32_e32 v141, s0, v141
	v_mul_f32_e32 v142, s0, v142
	v_mul_f32_e32 v143, s0, v143
	v_mul_f32_e32 v144, s0, v144
	v_mul_f32_e32 v145, s0, v145
	v_mul_f32_e32 v146, s0, v146
	v_mul_f32_e32 v147, s0, v147
	v_cvt_pk_fp8_f32 v132, v132, v136
	v_cvt_pk_fp8_f32 v133, v133, v137
	v_cvt_pk_fp8_f32 v134, v134, v138
	v_cvt_pk_fp8_f32 v135, v135, v139
	v_cvt_pk_fp8_f32 v132, v140, v144 op_sel:[0,0,1]
	v_cvt_pk_fp8_f32 v133, v141, v145 op_sel:[0,0,1]
	v_cvt_pk_fp8_f32 v134, v142, v146 op_sel:[0,0,1]
	v_cvt_pk_fp8_f32 v135, v143, v147 op_sel:[0,0,1]
	v_and_b32_e32 v136, 63, v0
	v_and_b32_e32 v138, 7, v136
	v_lshrrev_b32_e32 v136, 3, v136
	v_lshlrev_b32_e32 v136, 2, v136
	v_lshlrev_b32_e32 v137, 4, v138
	v_lshlrev_b32_e32 v138, 2, v138
	v_mad_u32_u24 v137, v138, s1, v136
	global_store_dword v137, v132, s[32:33] nt
	v_add_u32_e32 v136, s1, v137
	global_store_dword v136, v133, s[32:33] nt
	v_add_u32_e32 v138, s1, v136
	global_store_dword v138, v134, s[32:33] nt
	v_add_u32_e32 v139, s1, v138
	global_store_dword v139, v135, s[32:33] nt
.Lcn_snone_lfC:
	s_bitset0_b32 s101, 30
	s_bitcmp1_b32 s28, 31
	s_cbranch_scc0 .Lcn_snone_lfD
	s_and_b32 s8, s28, 0x3fffffff
	s_mul_i32 s9, s8, 0x2493
	s_lshr_b32 s9, s9, 16
	s_mul_i32 s10, s9, 7
	s_sub_u32 s10, s8, s10
	s_lshl_b32 s10, s10, 8
	s_lshr_b32 s11, s100, 3
	s_add_u32 s10, s10, s11
	s_and_b32 s8, s100, 7
	s_cmp_ge_u32 s9, 16
	s_cbranch_scc1 .Lcn_dn_lfDd
	s_lshr_b32 s11, s10, 4
	s_mul_i32 s11, s11, 0x2493
	s_lshr_b32 s11, s11, 16
	s_mul_i32 s12, s11, 0x70
	s_sub_u32 s12, s10, s12
	s_lshr_b32 s10, s8, 1
	s_lshl_b32 s11, s11, 2
	s_add_u32 s11, s11, s10
	s_and_b32 s8, s8, 1
	s_lshl_b32 s12, s12, 1
	s_add_u32 s12, s12, s8
	s_and_b32 s10, s9, 1
	s_lshr_b32 s9, s9, 1
	s_mul_i32 s8, s9, 0x1c00000
	s_add_u32 s8, s8, 0x4a000000
	s_lshr_b32 s9, s12, 2
	s_lshl_b32 s9, s9, 8
	s_lshl_b32 s10, s10, 7
	s_add_u32 s9, s9, s10
	s_and_b32 s10, s12, 3
	s_lshl_b32 s10, s10, 5
	s_add_u32 s9, s9, s10
	s_lshl_b32 s9, s9, 11
	s_add_u32 s8, s8, s9
	s_lshl_b32 s9, s11, 5
	s_add_u32 s8, s8, s9
	v_readlane_b32 s32, v255, 52
	v_readlane_b32 s33, v255, 53
	s_add_u32 s32, s32, s8
	s_addc_u32 s33, s33, 0
	s_movk_i32 s1, 0x800
	s_mov_b32 s0, 0x42000000
	s_branch .Lcn_dd_lfDd

; __device__ __forceinline__ unsigned pk4_fp8(float a, float b, float c, float d) { int p = __builtin_amdgcn_cvt_pk_fp8_f32(a, b, 0, false); p = __builtin_amdgcn_cvt_pk_fp8_f32(c, d, p, true); return (unsigned)p; }
; __device__ __forceinline__ void witem_store(const WItem& w, const f32x4 (&v)[16]) {
;     if (!w.valid) return;
;     if (w.f8) {
; #pragma unroll
;         for (int j = 0; j < 4; ++j) { u32x4 o; const float sc = w.scale;
;             o.x = pk4_fp8(v[0][j] * sc, v[1][j] * sc, v[2][j] * sc, v[3][j] * sc); o.y = pk4_fp8(v[4][j] * sc, v[5][j] * sc, v[6][j] * sc, v[7][j] * sc);
;             o.z = pk4_fp8(v[8][j] * sc, v[9][j] * sc, v[10][j] * sc, v[11][j] * sc); o.w = pk4_fp8(v[12][j] * sc, v[13][j] * sc, v[14][j] * sc, v[15][j] * sc);
;             *(u32x4*)(w.dst + (size_t)witem_row(w.kind, w.n + j) * w.K + w.k0) = o; }
.Lcn_dd_lfDd:
	s_mov_b32 s28, 0
	s_bitset1_b32 s101, 30
	v_mul_f32_e32 v148, s0, v148
	v_mul_f32_e32 v149, s0, v149
	v_mul_f32_e32 v150, s0, v150
	v_mul_f32_e32 v151, s0, v151
	v_mul_f32_e32 v152, s0, v152
	v_mul_f32_e32 v153, s0, v153
	v_mul_f32_e32 v154, s0, v154
	v_mul_f32_e32 v155, s0, v155
	v_mul_f32_e32 v156, s0, v156
	v_mul_f32_e32 v157, s0, v157
	v_mul_f32_e32 v158, s0, v158
	v_mul_f32_e32 v159, s0, v159
	v_mul_f32_e32 v160, s0, v160
	v_mul_f32_e32 v161, s0, v161
	v_mul_f32_e32 v162, s0, v162
	v_mul_f32_e32 v163, s0, v163
	v_cvt_pk_fp8_f32 v148, v148, v152
	v_cvt_pk_fp8_f32 v149, v149, v153
	v_cvt_pk_fp8_f32 v150, v150, v154
	v_cvt_pk_fp8_f32 v151, v151, v155
	v_cvt_pk_fp8_f32 v148, v156, v160 op_sel:[0,0,1]
	v_cvt_pk_fp8_f32 v149, v157, v161 op_sel:[0,0,1]
	v_cvt_pk_fp8_f32 v150, v158, v162 op_sel:[0,0,1]
	v_cvt_pk_fp8_f32 v151, v159, v163 op_sel:[0,0,1]
	v_and_b32_e32 v152, 63, v0
	v_and_b32_e32 v154, 7, v152
	v_lshrrev_b32_e32 v152, 3, v152
	v_lshlrev_b32_e32 v152, 2, v152
	v_lshlrev_b32_e32 v153, 4, v154
	v_lshlrev_b32_e32 v154, 2, v154
	v_mad_u32_u24 v153, v154, s1, v152
	global_store_dword v153, v148, s[32:33] nt
	v_add_u32_e32 v152, s1, v153
	global_store_dword v152, v149, s[32:33] nt
	v_add_u32_e32 v154, s1, v152
	global_store_dword v154, v150, s[32:33] nt
	v_add_u32_e32 v155, s1, v154
	global_store_dword v155, v151, s[32:33] nt
